# v10
# speedup vs baseline: 1.0127x; 1.0127x over previous
.LBB0_13:
	s_endpgm
	s_nop 0
	s_nop 0
	s_nop 0
	s_nop 0
	s_nop 0
	s_nop 0
	s_nop 0
	s_nop 0
	s_nop 0
	s_nop 0
	s_nop 0
	s_nop 0
	s_nop 0
	s_nop 0
	s_nop 0
	s_nop 0
	s_nop 0
	s_nop 0
	s_endpgm

_Z12gemm_persistILi0ELi4096ELi32ELi112EEvPKDF16_S1_PvPKfS4_S4_S4_PDF16_S5_iii:
	s_load_dwordx4 s[16:19], s[0:1], 0x48
	s_load_dword s3, s[0:1], 0x58
	s_waitcnt lgkmcnt(0)
	v_readfirstlane_b32 s19, v0
	s_mul_i32 s4, s3, s17
	s_add_i32 s4, s4, s2
	s_cmpk_gt_i32 s4, 0xdff
	s_cbranch_scc1 .LBB1_30
	v_lshrrev_b32_e32 v1, 5, v0
	v_lshrrev_b32_e32 v4, 2, v0
	v_and_b32_e32 v1, 4, v1
	v_lshrrev_b32_e32 v2, 3, v0
	v_bfe_u32 v3, v0, 3, 2
	v_and_b32_e32 v4, 24, v4
	v_or3_b32 v3, v1, v3, v4
	v_or_b32_e32 v4, 64, v2
	s_movk_i32 s5, 0x60
	v_and_or_b32 v5, v4, s5, v3
	s_ashr_i32 s5, s4, 31
	s_lshr_b32 s5, s5, 29
	s_add_i32 s5, s4, s5
	s_lshr_b32 s30, s19, 6
	s_ashr_i32 s8, s5, 3
	s_and_b32 s5, s5, -8
	s_lshr_b32 s31, s19, 8
	s_lshl_b32 s10, s30, 10
	s_sub_i32 s4, s4, s5
	s_cmp_lt_i32 s4, 0
	s_movk_i32 s33, 0x1c1
	s_cselect_b32 s5, s33, 0x1c0
	s_mul_i32 s4, s5, s4
	s_add_i32 s4, s4, s8
	s_mul_hi_i32 s5, s4, 0x92492493
	s_add_i32 s5, s5, s4
	s_lshr_b32 s8, s5, 31
	s_ashr_i32 s5, s5, 9
	s_add_i32 s5, s5, s8
	s_lshl_b32 s8, s5, 3
	s_mulk_i32 s5, 0x380
	s_sub_i32 s4, s4, s5
	s_bfe_u32 s5, s4, 0x3001c
	s_add_i32 s5, s4, s5
	s_sext_i32_i16 s9, s5
	s_and_b32 s5, s5, 0xfff8
	s_sub_i32 s4, s4, s5
	s_load_dwordx4 s[20:23], s[0:1], 0x0
	s_load_dwordx2 s[6:7], s[0:1], 0x10
	s_sext_i32_i16 s4, s4
	s_lshr_b32 s28, s9, 3
	s_add_i32 s42, s8, s4
	s_ashr_i32 s43, s42, 31
	s_bfe_i64 s[4:5], s[28:29], 0x100000
	s_lshl_b64 s[8:9], s[42:43], 21
	s_lshl_b64 s[4:5], s[4:5], 21
	v_xor_b32_e32 v1, v2, v0
	s_waitcnt lgkmcnt(0)
	s_add_u32 s4, s22, s4
	v_lshlrev_b32_e32 v1, 4, v1
	s_addc_u32 s5, s23, s5
	s_add_i32 s43, s10, 0
	v_and_b32_e32 v1, 0x70, v1
	v_and_or_b32 v3, v2, 32, v3
	s_add_i32 s52, s43, 0x10000
	s_add_i32 s53, s43, 0x12000
	v_lshl_or_b32 v200, v3, 13, v1
	s_mov_b32 m0, s52
	s_add_u32 s44, s20, s8
	v_lshl_or_b32 v196, v5, 13, v1
	v_lshlrev_b32_e32 v2, 13, v2
	global_load_lds_dwordx4 v200, s[4:5]
	s_mov_b32 m0, s53
	s_addc_u32 s45, s21, s9
	s_add_i32 s54, s43, 0x2000
	v_or_b32_e32 v202, v2, v1
	global_load_lds_dwordx4 v196, s[4:5]
	s_mov_b32 m0, s43
	s_add_u32 s8, s4, 0x100000
	v_lshl_or_b32 v198, v4, 13, v1
	global_load_lds_dwordx4 v202, s[44:45]
	s_mov_b32 m0, s54
	s_addc_u32 s9, s5, 0
	s_add_i32 s55, s43, 0x14000
	global_load_lds_dwordx4 v198, s[44:45]
	s_mov_b32 m0, s55
	s_add_i32 s56, s43, 0x16000
	global_load_lds_dwordx4 v200, s[8:9]
	s_mov_b32 m0, s56
	v_mov_b32_e32 v205, 0
	global_load_lds_dwordx4 v196, s[8:9]
	s_add_u32 s8, s44, 0x100000
	s_addc_u32 s9, s45, 0
	s_add_i32 s57, s43, 0x4000
	v_mov_b32_e32 v201, v205
	s_mov_b32 m0, s57
	s_add_i32 s58, s43, 0x6000
	v_lshl_add_u64 v[4:5], s[4:5], 0, v[200:201]
	v_mov_b32_e32 v197, v205
	global_load_lds_dwordx4 v202, s[8:9]
	s_mov_b32 m0, s58
	s_add_i32 s59, s43, 0x18000
	s_mov_b64 s[24:25], 0x80
	v_lshl_add_u64 v[6:7], s[4:5], 0, v[196:197]
	v_mov_b32_e32 v203, v205
	global_load_lds_dwordx4 v198, s[8:9]
	v_lshl_add_u64 v[4:5], v[4:5], 0, s[24:25]
	s_mov_b32 m0, s59
	s_add_i32 s60, s43, 0x1a000
	v_lshl_add_u64 v[8:9], s[44:45], 0, v[202:203]
	v_mov_b32_e32 v199, v205
	global_load_lds_dwordx4 v[4:5], off
	v_lshl_add_u64 v[4:5], v[6:7], 0, s[24:25]
	s_mov_b32 m0, s60
	s_add_i32 s61, s43, 0x8000
	s_add_i32 s62, s43, 0xa000
	v_lshl_add_u64 v[10:11], s[44:45], 0, v[198:199]
	global_load_lds_dwordx4 v[4:5], off
	v_lshl_add_u64 v[4:5], v[8:9], 0, s[24:25]
	s_mov_b32 m0, s61
	s_add_u32 s8, s4, 0x100080
	global_load_lds_dwordx4 v[4:5], off
	v_lshl_add_u64 v[4:5], v[10:11], 0, s[24:25]
	s_mov_b32 m0, s62
	s_addc_u32 s9, s5, 0
	s_add_i32 s63, s43, 0x1c000
	global_load_lds_dwordx4 v[4:5], off
	s_mov_b32 m0, s63
	s_add_i32 s64, s43, 0x1e000
	global_load_lds_dwordx4 v200, s[8:9]
	s_mov_b32 m0, s64
	s_mov_b32 s29, 0
	global_load_lds_dwordx4 v196, s[8:9]
	s_load_dwordx2 s[26:27], s[0:1], 0x40
	s_load_dwordx8 s[8:15], s[0:1], 0x20
	s_waitcnt vmcnt(6)
	s_cmp_lg_u32 s31, 1
	s_barrier
	v_lshrrev_b32_e32 v3, 4, v0
	v_and_b32_e32 v4, 15, v0
	v_bfe_u32 v5, v0, 4, 2
	v_and_b32_e32 v7, 7, v0
	s_lshl_b32 s0, s30, 5
	s_sext_i32_i16 s76, s28
	v_lshl_or_b32 v207, s31, 6, v4
	v_bitop3_b32 v3, v3, v7, 3 bitop3:0x6c
	v_bitop3_b32 v7, v5, v7, 4 bitop3:0x36
	s_and_b32 s28, s0, 0x60
	v_lshlrev_b32_e32 v6, 7, v207
	v_lshlrev_b32_e32 v3, 4, v3
	v_lshlrev_b32_e32 v7, 4, v7
	v_or_b32_e32 v4, s28, v4
	s_cmp_lg_u32 s16, 0
	v_lshlrev_b32_e32 v206, 2, v0
	v_lshlrev_b32_e32 v0, 4, v0
	v_or_b32_e32 v8, v6, v3
	v_or_b32_e32 v6, v6, v7
	v_lshlrev_b32_e32 v4, 7, v4
	s_cselect_b64 s[0:1], -1, 0
	v_add_u32_e32 v208, v2, v1
	v_add_u32_e32 v0, 0, v0
	v_or_b32_e32 v222, v4, v3
	v_or_b32_e32 v223, v4, v7
	s_mul_i32 s65, s2, 0x70
	v_lshl_or_b32 v224, v5, 3, s28
	v_add_u32_e32 v210, 0x80000, v208
	v_mov_b32_e32 v211, v205
	v_mov_b32_e32 v209, v205
	s_and_b64 s[0:1], exec, s[0:1]
	s_movk_i32 s16, 0xe00
	v_add_u32_e32 v225, 0x20000, v0
	s_add_i32 s66, 0, 0x10000
	s_add_i32 s67, 0, 0x10800
	s_add_i32 s68, 0, 0x14000
	s_add_i32 s69, 0, 0x14800
	s_add_i32 s70, 0, 0x18000
	s_add_i32 s71, 0, 0x18800
	s_add_i32 s72, 0, 0x1c000
	s_add_i32 s73, 0, 0x1c800
	s_movk_i32 s74, 0x7000
	v_add_u32_e32 v226, 0, v8
	v_add_u32_e32 v227, 0, v6
	s_mov_b32 s30, s29
	s_mov_b32 s34, s29
	s_mov_b32 s28, 0
	s_branch .LBB1_5

.LBB1_8:
	s_ashr_i32 s31, s30, 31
	s_xor_b64 s[38:39], s[46:47], -1
	s_lshl_b64 s[36:37], s[30:31], 21
	s_add_u32 s36, s20, s36
	s_addc_u32 s37, s21, s37
	s_and_b64 s[40:41], s[46:47], exec
	s_cselect_b32 s31, s37, s45
	s_cselect_b32 s77, s36, s44
	s_ashr_i32 s35, s34, 31
	s_lshl_b64 s[40:41], s[34:35], 21
	s_add_u32 s40, s22, s40
	s_addc_u32 s41, s23, s41
	s_and_b64 s[46:47], s[46:47], exec
	s_cselect_b32 s35, s41, s5
	s_cselect_b32 s78, s40, s4
	s_lshl_b32 s79, s28, 4
	s_add_i32 s79, s79, s65
	s_add_u32 s80, s4, 0x100
	s_addc_u32 s81, s5, 0
	s_add_u32 s44, s44, 0x100080
	v_mov_b32_e32 v4, 0
	s_addc_u32 s45, s45, 0
	s_mov_b32 s48, -2
	v_mov_b32_e32 v5, v4
	v_mov_b32_e32 v6, v4
	v_mov_b32_e32 v7, v4
	v_mov_b32_e32 v12, v4
	v_mov_b32_e32 v13, v4
	v_mov_b32_e32 v14, v4
	v_mov_b32_e32 v15, v4
	v_mov_b32_e32 v20, v4
	v_mov_b32_e32 v21, v4
	v_mov_b32_e32 v22, v4
	v_mov_b32_e32 v23, v4
	v_mov_b32_e32 v28, v4
	v_mov_b32_e32 v29, v4
	v_mov_b32_e32 v30, v4
	v_mov_b32_e32 v31, v4
	v_mov_b32_e32 v36, v4
	v_mov_b32_e32 v37, v4
	v_mov_b32_e32 v38, v4
	v_mov_b32_e32 v39, v4
	v_mov_b32_e32 v44, v4
	v_mov_b32_e32 v45, v4
	v_mov_b32_e32 v46, v4
	v_mov_b32_e32 v47, v4
	v_mov_b32_e32 v52, v4
	v_mov_b32_e32 v53, v4
	v_mov_b32_e32 v54, v4
	v_mov_b32_e32 v55, v4
	v_mov_b32_e32 v60, v4
	v_mov_b32_e32 v61, v4
	v_mov_b32_e32 v62, v4
	v_mov_b32_e32 v63, v4
	v_mov_b32_e32 v8, v4
	v_mov_b32_e32 v9, v4
	v_mov_b32_e32 v10, v4
	v_mov_b32_e32 v11, v4
	v_mov_b32_e32 v16, v4
	v_mov_b32_e32 v17, v4
	v_mov_b32_e32 v18, v4
	v_mov_b32_e32 v19, v4
	v_mov_b32_e32 v24, v4
	v_mov_b32_e32 v25, v4
	v_mov_b32_e32 v26, v4
	v_mov_b32_e32 v27, v4
	v_mov_b32_e32 v32, v4
	v_mov_b32_e32 v33, v4
	v_mov_b32_e32 v34, v4
	v_mov_b32_e32 v35, v4
	v_mov_b32_e32 v40, v4
	v_mov_b32_e32 v41, v4
	v_mov_b32_e32 v42, v4
	v_mov_b32_e32 v43, v4
	v_mov_b32_e32 v48, v4
	v_mov_b32_e32 v49, v4
	v_mov_b32_e32 v50, v4
	v_mov_b32_e32 v51, v4
	v_mov_b32_e32 v56, v4
	v_mov_b32_e32 v57, v4
	v_mov_b32_e32 v58, v4
	v_mov_b32_e32 v59, v4
	v_mov_b32_e32 v64, v4
	v_mov_b32_e32 v65, v4
	v_mov_b32_e32 v66, v4
	v_mov_b32_e32 v67, v4
	v_mov_b32_e32 v68, v4
	v_mov_b32_e32 v69, v4
	v_mov_b32_e32 v70, v4
	v_mov_b32_e32 v71, v4
	v_mov_b32_e32 v76, v4
	v_mov_b32_e32 v77, v4
	v_mov_b32_e32 v78, v4
	v_mov_b32_e32 v79, v4
	v_mov_b32_e32 v84, v4
	v_mov_b32_e32 v85, v4
	v_mov_b32_e32 v86, v4
	v_mov_b32_e32 v87, v4
	v_mov_b32_e32 v92, v4
	v_mov_b32_e32 v93, v4
	v_mov_b32_e32 v94, v4
	v_mov_b32_e32 v95, v4
	v_mov_b32_e32 v100, v4
	v_mov_b32_e32 v101, v4
	v_mov_b32_e32 v102, v4
	v_mov_b32_e32 v103, v4
	v_mov_b32_e32 v108, v4
	v_mov_b32_e32 v109, v4
	v_mov_b32_e32 v110, v4
	v_mov_b32_e32 v111, v4
	v_mov_b32_e32 v116, v4
	v_mov_b32_e32 v117, v4
	v_mov_b32_e32 v118, v4
	v_mov_b32_e32 v119, v4
	v_mov_b32_e32 v124, v4
	v_mov_b32_e32 v125, v4
	v_mov_b32_e32 v126, v4
	v_mov_b32_e32 v127, v4
	v_mov_b32_e32 v72, v4
	v_mov_b32_e32 v73, v4
	v_mov_b32_e32 v74, v4
	v_mov_b32_e32 v75, v4
	v_mov_b32_e32 v80, v4
	v_mov_b32_e32 v81, v4
	v_mov_b32_e32 v82, v4
	v_mov_b32_e32 v83, v4
	v_mov_b32_e32 v88, v4
	v_mov_b32_e32 v89, v4
	v_mov_b32_e32 v90, v4
	v_mov_b32_e32 v91, v4
	v_mov_b32_e32 v96, v4
	v_mov_b32_e32 v97, v4
	v_mov_b32_e32 v98, v4
	v_mov_b32_e32 v99, v4
	v_mov_b32_e32 v104, v4
	v_mov_b32_e32 v105, v4
	v_mov_b32_e32 v106, v4
	v_mov_b32_e32 v107, v4
	v_mov_b32_e32 v112, v4
	v_mov_b32_e32 v113, v4
	v_mov_b32_e32 v114, v4
	v_mov_b32_e32 v115, v4
	v_mov_b32_e32 v120, v4
	v_mov_b32_e32 v121, v4
	v_mov_b32_e32 v122, v4
	v_mov_b32_e32 v123, v4
	v_mov_b32_e32 v128, v4
	v_mov_b32_e32 v129, v4
	v_mov_b32_e32 v130, v4
	v_mov_b32_e32 v131, v4
	s_cmpk_gt_u32 s19, 0xff
	s_cbranch_scc1 .Lk1y_9

.Lk1x_14:
	v_add_u32_e32 v132, s66, v222
	v_add_u32_e32 v133, s66, v223
	ds_read_b128 v[148:151], v132
	ds_read_b128 v[152:155], v133
	v_add_u32_e32 v132, s67, v222
	v_add_u32_e32 v133, s67, v223
	ds_read_b128 v[156:159], v132
	ds_read_b128 v[160:163], v133
	v_add_u32_e32 v132, s68, v222
	v_add_u32_e32 v136, s68, v223
	v_add_u32_e32 v140, s69, v222
	v_add_u32_e32 v144, s69, v223
	v_lshl_add_u64 v[194:195], s[44:45], 0, v[208:209]
	s_add_i32 m0, s43, 0xc000
	ds_read_b128 v[132:135], v132
	ds_read_b128 v[136:139], v136
	ds_read_b128 v[140:143], v140
	ds_read_b128 v[144:147], v144
	ds_read_b128 v[166:169], v226
	ds_read_b128 v[170:173], v226 offset:2048
	ds_read_b128 v[174:177], v227
	ds_read_b128 v[178:181], v227 offset:2048
	ds_read_b128 v[182:185], v226 offset:4096
	ds_read_b128 v[186:189], v226 offset:6144
	ds_read_b128 v[190:193], v227 offset:4096
	ds_read_b128 v[214:217], v227 offset:6144
	global_load_lds_dwordx4 v[194:195], off
	v_lshl_add_u64 v[194:195], s[44:45], 0, v[210:211]
	s_add_i32 m0, s43, 0xe000
	s_nop 0
	global_load_lds_dwordx4 v[194:195], off
	s_waitcnt vmcnt(8)
	s_waitcnt lgkmcnt(0)
	s_setprio 1
	s_waitcnt lgkmcnt(0)
	v_mfma_f32_16x16x32_f16 v[128:131], v[148:151], v[166:169], v[128:131]
	v_mfma_f32_16x16x32_f16 v[128:131], v[152:155], v[174:177], v[128:131]
	v_mfma_f32_16x16x32_f16 v[120:123], v[156:159], v[166:169], v[120:123]
	v_mfma_f32_16x16x32_f16 v[120:123], v[160:163], v[174:177], v[120:123]
	v_mfma_f32_16x16x32_f16 v[112:115], v[148:151], v[170:173], v[112:115]
	v_mfma_f32_16x16x32_f16 v[112:115], v[152:155], v[178:181], v[112:115]
	v_mfma_f32_16x16x32_f16 v[104:107], v[156:159], v[170:173], v[104:107]
	v_mfma_f32_16x16x32_f16 v[104:107], v[160:163], v[178:181], v[104:107]
	v_mfma_f32_16x16x32_f16 v[96:99], v[148:151], v[182:185], v[96:99]
	v_mfma_f32_16x16x32_f16 v[96:99], v[152:155], v[190:193], v[96:99]
	v_mfma_f32_16x16x32_f16 v[88:91], v[156:159], v[182:185], v[88:91]
	v_mfma_f32_16x16x32_f16 v[88:91], v[160:163], v[190:193], v[88:91]
	v_mfma_f32_16x16x32_f16 v[80:83], v[148:151], v[186:189], v[80:83]
	v_mfma_f32_16x16x32_f16 v[80:83], v[152:155], v[214:217], v[80:83]
	v_mfma_f32_16x16x32_f16 v[72:75], v[156:159], v[186:189], v[72:75]
	v_mfma_f32_16x16x32_f16 v[72:75], v[160:163], v[214:217], v[72:75]
	s_setprio 0
	s_setprio 1
	v_mfma_f32_16x16x32_f16 v[124:127], v[132:135], v[166:169], v[124:127]
	v_mfma_f32_16x16x32_f16 v[124:127], v[136:139], v[174:177], v[124:127]
	v_mfma_f32_16x16x32_f16 v[116:119], v[140:143], v[166:169], v[116:119]
	v_mfma_f32_16x16x32_f16 v[116:119], v[144:147], v[174:177], v[116:119]
	v_mfma_f32_16x16x32_f16 v[108:111], v[132:135], v[170:173], v[108:111]
	v_mfma_f32_16x16x32_f16 v[108:111], v[136:139], v[178:181], v[108:111]
	v_mfma_f32_16x16x32_f16 v[100:103], v[140:143], v[170:173], v[100:103]
	v_mfma_f32_16x16x32_f16 v[100:103], v[144:147], v[178:181], v[100:103]
	v_mfma_f32_16x16x32_f16 v[92:95], v[132:135], v[182:185], v[92:95]
	v_mfma_f32_16x16x32_f16 v[92:95], v[136:139], v[190:193], v[92:95]
	v_mfma_f32_16x16x32_f16 v[84:87], v[140:143], v[182:185], v[84:87]
	v_mfma_f32_16x16x32_f16 v[84:87], v[144:147], v[190:193], v[84:87]
	v_mfma_f32_16x16x32_f16 v[76:79], v[132:135], v[186:189], v[76:79]
	v_mfma_f32_16x16x32_f16 v[76:79], v[136:139], v[214:217], v[76:79]
	v_mfma_f32_16x16x32_f16 v[68:71], v[140:143], v[186:189], v[68:71]
	v_mfma_f32_16x16x32_f16 v[68:71], v[144:147], v[214:217], v[68:71]
	s_setprio 0
	s_barrier
	s_andn2_b64 vcc, exec, s[4:5]
	s_cbranch_vccnz .Lk1x_16
	v_cvt_pkrtz_f16_f32 v166, v0, v1
	v_cvt_pkrtz_f16_f32 v167, v2, v3
	v_add_u32_e32 v166, 0x20002, v166
	v_add_u32_e32 v167, 0x20002, v167
	v_and_b32_e32 v166, 0xfffcfffc, v166
	v_and_b32_e32 v167, 0xfffcfffc, v167
	global_store_dwordx2 v[164:165], v[166:167], off

.Lk1x_20:
	s_waitcnt lgkmcnt(0)
	s_setprio 1
	s_waitcnt lgkmcnt(0)
	v_mfma_f32_16x16x32_f16 v[64:67], v[148:151], v[188:191], v[64:67]
	v_mfma_f32_16x16x32_f16 v[64:67], v[152:155], v[192:195], v[64:67]
	v_mfma_f32_16x16x32_f16 v[56:59], v[156:159], v[188:191], v[56:59]
	v_mfma_f32_16x16x32_f16 v[56:59], v[160:163], v[192:195], v[56:59]
	v_mfma_f32_16x16x32_f16 v[48:51], v[148:151], v[176:179], v[48:51]
	v_mfma_f32_16x16x32_f16 v[48:51], v[152:155], v[180:183], v[48:51]
	v_mfma_f32_16x16x32_f16 v[40:43], v[156:159], v[176:179], v[40:43]
	v_mfma_f32_16x16x32_f16 v[40:43], v[160:163], v[180:183], v[40:43]
	v_mfma_f32_16x16x32_f16 v[32:35], v[148:151], v[172:175], v[32:35]
	v_mfma_f32_16x16x32_f16 v[32:35], v[152:155], v[184:187], v[32:35]
	v_mfma_f32_16x16x32_f16 v[24:27], v[156:159], v[172:175], v[24:27]
	v_mfma_f32_16x16x32_f16 v[24:27], v[160:163], v[184:187], v[24:27]
	v_mfma_f32_16x16x32_f16 v[16:19], v[148:151], v[164:167], v[16:19]
	v_mfma_f32_16x16x32_f16 v[16:19], v[152:155], v[168:171], v[16:19]
	v_mfma_f32_16x16x32_f16 v[8:11], v[156:159], v[164:167], v[8:11]
	v_mfma_f32_16x16x32_f16 v[8:11], v[160:163], v[168:171], v[8:11]
	s_setprio 0
	s_setprio 1
	v_mfma_f32_16x16x32_f16 v[60:63], v[132:135], v[188:191], v[60:63]
	v_mfma_f32_16x16x32_f16 v[60:63], v[136:139], v[192:195], v[60:63]
	v_mfma_f32_16x16x32_f16 v[52:55], v[140:143], v[188:191], v[52:55]
	v_mfma_f32_16x16x32_f16 v[52:55], v[144:147], v[192:195], v[52:55]
	v_mfma_f32_16x16x32_f16 v[44:47], v[132:135], v[176:179], v[44:47]
	v_mfma_f32_16x16x32_f16 v[44:47], v[136:139], v[180:183], v[44:47]
	v_mfma_f32_16x16x32_f16 v[36:39], v[140:143], v[176:179], v[36:39]
	v_mfma_f32_16x16x32_f16 v[36:39], v[144:147], v[180:183], v[36:39]
	v_mfma_f32_16x16x32_f16 v[28:31], v[132:135], v[172:175], v[28:31]
	v_mfma_f32_16x16x32_f16 v[28:31], v[136:139], v[184:187], v[28:31]
	v_mfma_f32_16x16x32_f16 v[20:23], v[140:143], v[172:175], v[20:23]
	v_mfma_f32_16x16x32_f16 v[20:23], v[144:147], v[184:187], v[20:23]
	v_mfma_f32_16x16x32_f16 v[12:15], v[132:135], v[164:167], v[12:15]
	v_mfma_f32_16x16x32_f16 v[12:15], v[136:139], v[168:171], v[12:15]
	v_mfma_f32_16x16x32_f16 v[4:7], v[140:143], v[164:167], v[4:7]
	v_mfma_f32_16x16x32_f16 v[4:7], v[144:147], v[168:171], v[4:7]
	s_setprio 0
	s_barrier
	v_add_u32_e32 v132, s70, v222
	s_add_u32 s48, s48, 0x100000
	v_add_u32_e32 v133, s70, v223
	ds_read_b128 v[148:151], v132
	ds_read_b128 v[152:155], v133
	v_add_u32_e32 v132, s71, v222
	s_addc_u32 s49, s49, 0
	s_mov_b32 m0, s57
	v_add_u32_e32 v133, s71, v223
	ds_read_b128 v[156:159], v132
	ds_read_b128 v[160:163], v133
	v_add_u32_e32 v132, s72, v222
	v_add_u32_e32 v136, s72, v223
	v_add_u32_e32 v140, s73, v222
	v_add_u32_e32 v144, s73, v223
	v_lshl_add_u64 v[212:213], s[48:49], 0, v[202:203]
	ds_read_b128 v[132:135], v132
	ds_read_b128 v[136:139], v136
	ds_read_b128 v[140:143], v140
	ds_read_b128 v[144:147], v144
	ds_read_b128 v[188:191], v226 offset:32768
	ds_read_b128 v[176:179], v226 offset:34816
	ds_read_b128 v[192:195], v227 offset:32768
	ds_read_b128 v[180:183], v227 offset:34816
	ds_read_b128 v[172:175], v226 offset:36864
	ds_read_b128 v[164:167], v226 offset:38912
	ds_read_b128 v[184:187], v227 offset:36864
	ds_read_b128 v[168:171], v227 offset:38912
	global_load_lds_dwordx4 v[212:213], off
	v_lshl_add_u64 v[212:213], s[48:49], 0, v[198:199]
	s_mov_b32 m0, s58
	s_mov_b64 s[48:49], -1
	global_load_lds_dwordx4 v[212:213], off
	s_mov_b64 vcc, s[4:5]
	s_cbranch_vccz .Lk1x_22
	s_waitcnt vmcnt(8)
	s_mov_b64 s[48:49], 0

.Lk1x_24:
	s_waitcnt lgkmcnt(0)
	s_setprio 1
	s_waitcnt lgkmcnt(0)
	v_mfma_f32_16x16x32_f16 v[128:131], v[148:151], v[188:191], v[128:131]
	v_mfma_f32_16x16x32_f16 v[128:131], v[152:155], v[192:195], v[128:131]
	v_mfma_f32_16x16x32_f16 v[120:123], v[156:159], v[188:191], v[120:123]
	v_mfma_f32_16x16x32_f16 v[120:123], v[160:163], v[192:195], v[120:123]
	v_mfma_f32_16x16x32_f16 v[112:115], v[148:151], v[176:179], v[112:115]
	v_mfma_f32_16x16x32_f16 v[112:115], v[152:155], v[180:183], v[112:115]
	v_mfma_f32_16x16x32_f16 v[104:107], v[156:159], v[176:179], v[104:107]
	v_mfma_f32_16x16x32_f16 v[104:107], v[160:163], v[180:183], v[104:107]
	v_mfma_f32_16x16x32_f16 v[96:99], v[148:151], v[172:175], v[96:99]
	v_mfma_f32_16x16x32_f16 v[96:99], v[152:155], v[184:187], v[96:99]
	v_mfma_f32_16x16x32_f16 v[88:91], v[156:159], v[172:175], v[88:91]
	v_mfma_f32_16x16x32_f16 v[88:91], v[160:163], v[184:187], v[88:91]
	v_mfma_f32_16x16x32_f16 v[80:83], v[148:151], v[164:167], v[80:83]
	v_mfma_f32_16x16x32_f16 v[80:83], v[152:155], v[168:171], v[80:83]
	v_mfma_f32_16x16x32_f16 v[72:75], v[156:159], v[164:167], v[72:75]
	v_mfma_f32_16x16x32_f16 v[72:75], v[160:163], v[168:171], v[72:75]
	s_setprio 0
	s_setprio 1
	v_mfma_f32_16x16x32_f16 v[124:127], v[132:135], v[188:191], v[124:127]
	v_mfma_f32_16x16x32_f16 v[124:127], v[136:139], v[192:195], v[124:127]
	v_mfma_f32_16x16x32_f16 v[116:119], v[140:143], v[188:191], v[116:119]
	v_mfma_f32_16x16x32_f16 v[116:119], v[144:147], v[192:195], v[116:119]
	v_mfma_f32_16x16x32_f16 v[108:111], v[132:135], v[176:179], v[108:111]
	v_mfma_f32_16x16x32_f16 v[108:111], v[136:139], v[180:183], v[108:111]
	v_mfma_f32_16x16x32_f16 v[100:103], v[140:143], v[176:179], v[100:103]
	v_mfma_f32_16x16x32_f16 v[100:103], v[144:147], v[180:183], v[100:103]
	v_mfma_f32_16x16x32_f16 v[92:95], v[132:135], v[172:175], v[92:95]
	v_mfma_f32_16x16x32_f16 v[92:95], v[136:139], v[184:187], v[92:95]
	v_mfma_f32_16x16x32_f16 v[84:87], v[140:143], v[172:175], v[84:87]
	v_mfma_f32_16x16x32_f16 v[84:87], v[144:147], v[184:187], v[84:87]
	v_mfma_f32_16x16x32_f16 v[76:79], v[132:135], v[164:167], v[76:79]
	v_mfma_f32_16x16x32_f16 v[76:79], v[136:139], v[168:171], v[76:79]
	v_mfma_f32_16x16x32_f16 v[68:71], v[140:143], v[164:167], v[68:71]
	v_mfma_f32_16x16x32_f16 v[68:71], v[144:147], v[168:171], v[68:71]
	s_setprio 0
	s_barrier
	s_mov_b32 m0, s59
	v_lshl_add_u64 v[212:213], v[214:215], 0, s[24:25]
	s_add_u32 s4, s46, 0x100080
	ds_read_b128 v[164:167], v226 offset:49152
	ds_read_b128 v[168:171], v226 offset:51200
	ds_read_b128 v[172:175], v227 offset:49152
	ds_read_b128 v[176:179], v227 offset:51200
	ds_read_b128 v[180:183], v226 offset:53248
	ds_read_b128 v[184:187], v226 offset:55296
	ds_read_b128 v[188:191], v227 offset:53248
	ds_read_b128 v[192:195], v227 offset:55296
	global_load_lds_dwordx4 v[212:213], off
	v_lshl_add_u64 v[212:213], v[216:217], 0, s[24:25]
	s_mov_b32 m0, s60
	s_addc_u32 s5, s47, 0
	global_load_lds_dwordx4 v[212:213], off
	v_lshl_add_u64 v[212:213], s[4:5], 0, v[200:201]
	s_mov_b32 m0, s63
	s_nop 0
	global_load_lds_dwordx4 v[212:213], off
	v_lshl_add_u64 v[212:213], s[4:5], 0, v[196:197]
	s_mov_b32 m0, s64
	s_nop 0
	global_load_lds_dwordx4 v[212:213], off
	v_lshl_add_u64 v[212:213], v[218:219], 0, s[24:25]
	s_mov_b32 m0, s61
	s_nop 0
	global_load_lds_dwordx4 v[212:213], off
	v_lshl_add_u64 v[212:213], v[220:221], 0, s[24:25]
	s_mov_b32 m0, s62
	s_nop 0
	global_load_lds_dwordx4 v[212:213], off
	s_waitcnt vmcnt(8)
	s_waitcnt lgkmcnt(0)
	s_setprio 1
	s_waitcnt lgkmcnt(0)
	v_mfma_f32_16x16x32_f16 v[64:67], v[148:151], v[164:167], v[64:67]
	v_mfma_f32_16x16x32_f16 v[64:67], v[152:155], v[172:175], v[64:67]
	v_mfma_f32_16x16x32_f16 v[56:59], v[156:159], v[164:167], v[56:59]
	v_mfma_f32_16x16x32_f16 v[56:59], v[160:163], v[172:175], v[56:59]
	v_mfma_f32_16x16x32_f16 v[48:51], v[148:151], v[168:171], v[48:51]
	v_mfma_f32_16x16x32_f16 v[48:51], v[152:155], v[176:179], v[48:51]
	v_mfma_f32_16x16x32_f16 v[40:43], v[156:159], v[168:171], v[40:43]
	v_mfma_f32_16x16x32_f16 v[40:43], v[160:163], v[176:179], v[40:43]
	v_mfma_f32_16x16x32_f16 v[32:35], v[148:151], v[180:183], v[32:35]
	v_mfma_f32_16x16x32_f16 v[32:35], v[152:155], v[188:191], v[32:35]
	v_mfma_f32_16x16x32_f16 v[24:27], v[156:159], v[180:183], v[24:27]
	v_mfma_f32_16x16x32_f16 v[24:27], v[160:163], v[188:191], v[24:27]
	v_mfma_f32_16x16x32_f16 v[16:19], v[148:151], v[184:187], v[16:19]
	v_mfma_f32_16x16x32_f16 v[16:19], v[152:155], v[192:195], v[16:19]
	v_mfma_f32_16x16x32_f16 v[8:11], v[156:159], v[184:187], v[8:11]
	v_mfma_f32_16x16x32_f16 v[8:11], v[160:163], v[192:195], v[8:11]
	s_setprio 0
	s_setprio 1
	v_mfma_f32_16x16x32_f16 v[60:63], v[132:135], v[164:167], v[60:63]
	v_mfma_f32_16x16x32_f16 v[60:63], v[136:139], v[172:175], v[60:63]
	v_mfma_f32_16x16x32_f16 v[52:55], v[140:143], v[164:167], v[52:55]
	v_mfma_f32_16x16x32_f16 v[52:55], v[144:147], v[172:175], v[52:55]
	v_mfma_f32_16x16x32_f16 v[44:47], v[132:135], v[168:171], v[44:47]
	v_mfma_f32_16x16x32_f16 v[44:47], v[136:139], v[176:179], v[44:47]
	v_mfma_f32_16x16x32_f16 v[36:39], v[140:143], v[168:171], v[36:39]
	v_mfma_f32_16x16x32_f16 v[36:39], v[144:147], v[176:179], v[36:39]
	v_mfma_f32_16x16x32_f16 v[28:31], v[132:135], v[180:183], v[28:31]
	v_mfma_f32_16x16x32_f16 v[28:31], v[136:139], v[188:191], v[28:31]
	v_mfma_f32_16x16x32_f16 v[20:23], v[140:143], v[180:183], v[20:23]
	v_mfma_f32_16x16x32_f16 v[20:23], v[144:147], v[188:191], v[20:23]
	v_mfma_f32_16x16x32_f16 v[12:15], v[132:135], v[184:187], v[12:15]
	v_mfma_f32_16x16x32_f16 v[12:15], v[136:139], v[192:195], v[12:15]
	v_mfma_f32_16x16x32_f16 v[4:7], v[140:143], v[184:187], v[4:7]
	v_mfma_f32_16x16x32_f16 v[4:7], v[144:147], v[192:195], v[4:7]
	s_setprio 0
	s_barrier
	s_add_u32 s80, s80, 0x100
	s_addc_u32 s81, s81, 0
	s_add_u32 s44, s44, 0x100
	s_addc_u32 s45, s45, 0
	s_cmp_gt_u32 s82, 61
	s_cbranch_scc1 .LBB1_4
	s_mov_b32 s48, s82
	s_branch .Lk1x_9
.Lk1x_26:
	s_branch .Lk1x_11
.Lk1y_9:
	s_add_i32 s82, s48, 2
	s_lshr_b32 s4, s82, 2
	s_add_i32 s4, s4, s79
	s_mov_b64 vcc, s[0:1]
	s_cbranch_vccz .Lk1y_26
	s_mul_hi_i32 s5, s4, 0x92492493
	s_add_i32 s5, s5, s4
	s_lshr_b32 s28, s5, 31
	s_ashr_i32 s5, s5, 12
	s_add_i32 s5, s5, s28
	s_mul_i32 s28, s5, 0x1c00
	s_sub_i32 s46, s4, s28
	s_bitcmp0_b32 s5, 0
	s_cselect_b32 s28, s16, 0x2a00
	s_ashr_i32 s49, s46, 1
	s_lshl_b32 s46, s46, 11
	s_add_i32 s28, s28, s49
	s_and_b32 s46, s46, 0x800
	s_cmp_lt_u32 s5, 2
	v_or_b32_e32 v132, s46, v206
	s_waitcnt lgkmcnt(0)
	s_cselect_b32 s50, s9, s11
	s_cselect_b32 s51, s8, s10
	s_lshl_b64 s[46:47], s[28:29], 14
	s_add_u32 s46, s51, s46
	s_addc_u32 s47, s50, s47
	v_lshlrev_b32_e32 v204, 2, v132
	s_lshl_b32 s5, s5, 6
	v_lshl_add_u64 v[212:213], s[46:47], 0, v[204:205]
	s_lshl_b32 s28, s28, 1
	s_and_b32 s46, s49, 0x7f
	s_and_b32 s5, s5, 0xffffff80
	s_and_b32 s28, s28, 0x7fffff00
	s_or_b32 s5, s5, s46
	s_add_i32 s46, s5, s28
	s_ashr_i32 s47, s46, 31
	s_lshl_b64 s[46:47], s[46:47], 13
	s_add_u32 s46, s14, s46
	s_addc_u32 s47, s15, s47
	v_lshlrev_b32_e32 v204, 1, v132
	v_lshl_add_u64 v[164:165], s[46:47], 0, v[204:205]
	s_cbranch_execnz .Lk1y_12

.Lk1y_14:
	v_add_u32_e32 v132, s66, v222
	v_add_u32_e32 v133, s66, v223
	ds_read_b128 v[148:151], v132
	ds_read_b128 v[152:155], v133
	v_add_u32_e32 v132, s67, v222
	v_add_u32_e32 v133, s67, v223
	ds_read_b128 v[156:159], v132
	ds_read_b128 v[160:163], v133
	v_add_u32_e32 v132, s68, v222
	v_add_u32_e32 v136, s68, v223
	v_add_u32_e32 v140, s69, v222
	v_add_u32_e32 v144, s69, v223
	v_lshl_add_u64 v[194:195], s[44:45], 0, v[208:209]
	s_add_i32 m0, s43, 0xc000
	ds_read_b128 v[132:135], v132
	ds_read_b128 v[136:139], v136
	ds_read_b128 v[140:143], v140
	ds_read_b128 v[144:147], v144
	ds_read_b128 v[166:169], v226
	ds_read_b128 v[170:173], v226 offset:2048
	ds_read_b128 v[174:177], v227
	ds_read_b128 v[178:181], v227 offset:2048
	ds_read_b128 v[182:185], v226 offset:4096
	ds_read_b128 v[186:189], v226 offset:6144
	ds_read_b128 v[190:193], v227 offset:4096
	ds_read_b128 v[214:217], v227 offset:6144
	global_load_lds_dwordx4 v[194:195], off
	v_lshl_add_u64 v[194:195], s[44:45], 0, v[210:211]
	s_add_i32 m0, s43, 0xe000
	s_nop 0
	global_load_lds_dwordx4 v[194:195], off
	s_waitcnt vmcnt(8)
	s_waitcnt lgkmcnt(0)
	s_barrier
	s_setprio 2
	s_waitcnt lgkmcnt(0)
	v_mfma_f32_16x16x32_f16 v[128:131], v[148:151], v[166:169], v[128:131]
	v_mfma_f32_16x16x32_f16 v[128:131], v[152:155], v[174:177], v[128:131]
	v_mfma_f32_16x16x32_f16 v[120:123], v[156:159], v[166:169], v[120:123]
	v_mfma_f32_16x16x32_f16 v[120:123], v[160:163], v[174:177], v[120:123]
	v_mfma_f32_16x16x32_f16 v[112:115], v[148:151], v[170:173], v[112:115]
	v_mfma_f32_16x16x32_f16 v[112:115], v[152:155], v[178:181], v[112:115]
	v_mfma_f32_16x16x32_f16 v[104:107], v[156:159], v[170:173], v[104:107]
	v_mfma_f32_16x16x32_f16 v[104:107], v[160:163], v[178:181], v[104:107]
	v_mfma_f32_16x16x32_f16 v[96:99], v[148:151], v[182:185], v[96:99]
	v_mfma_f32_16x16x32_f16 v[96:99], v[152:155], v[190:193], v[96:99]
	v_mfma_f32_16x16x32_f16 v[88:91], v[156:159], v[182:185], v[88:91]
	v_mfma_f32_16x16x32_f16 v[88:91], v[160:163], v[190:193], v[88:91]
	v_mfma_f32_16x16x32_f16 v[80:83], v[148:151], v[186:189], v[80:83]
	v_mfma_f32_16x16x32_f16 v[80:83], v[152:155], v[214:217], v[80:83]
	v_mfma_f32_16x16x32_f16 v[72:75], v[156:159], v[186:189], v[72:75]
	v_mfma_f32_16x16x32_f16 v[72:75], v[160:163], v[214:217], v[72:75]
	s_setprio 0
	s_setprio 2
	v_mfma_f32_16x16x32_f16 v[124:127], v[132:135], v[166:169], v[124:127]
	v_mfma_f32_16x16x32_f16 v[124:127], v[136:139], v[174:177], v[124:127]
	v_mfma_f32_16x16x32_f16 v[116:119], v[140:143], v[166:169], v[116:119]
	v_mfma_f32_16x16x32_f16 v[116:119], v[144:147], v[174:177], v[116:119]
	v_mfma_f32_16x16x32_f16 v[108:111], v[132:135], v[170:173], v[108:111]
	v_mfma_f32_16x16x32_f16 v[108:111], v[136:139], v[178:181], v[108:111]
	v_mfma_f32_16x16x32_f16 v[100:103], v[140:143], v[170:173], v[100:103]
	v_mfma_f32_16x16x32_f16 v[100:103], v[144:147], v[178:181], v[100:103]
	v_mfma_f32_16x16x32_f16 v[92:95], v[132:135], v[182:185], v[92:95]
	v_mfma_f32_16x16x32_f16 v[92:95], v[136:139], v[190:193], v[92:95]
	v_mfma_f32_16x16x32_f16 v[84:87], v[140:143], v[182:185], v[84:87]
	v_mfma_f32_16x16x32_f16 v[84:87], v[144:147], v[190:193], v[84:87]
	v_mfma_f32_16x16x32_f16 v[76:79], v[132:135], v[186:189], v[76:79]
	v_mfma_f32_16x16x32_f16 v[76:79], v[136:139], v[214:217], v[76:79]
	v_mfma_f32_16x16x32_f16 v[68:71], v[140:143], v[186:189], v[68:71]
	v_mfma_f32_16x16x32_f16 v[68:71], v[144:147], v[214:217], v[68:71]
	s_setprio 0
	s_andn2_b64 vcc, exec, s[4:5]
	s_cbranch_vccnz .Lk1y_16
	v_cvt_pkrtz_f16_f32 v166, v0, v1
	v_cvt_pkrtz_f16_f32 v167, v2, v3
	v_add_u32_e32 v166, 0x20002, v166
	v_add_u32_e32 v167, 0x20002, v167
	v_and_b32_e32 v166, 0xfffcfffc, v166
	v_and_b32_e32 v167, 0xfffcfffc, v167
	global_store_dwordx2 v[164:165], v[166:167], off

.Lk1y_20:
	s_waitcnt lgkmcnt(0)
	s_barrier
	s_setprio 2
	s_waitcnt lgkmcnt(0)
	v_mfma_f32_16x16x32_f16 v[64:67], v[148:151], v[188:191], v[64:67]
	v_mfma_f32_16x16x32_f16 v[64:67], v[152:155], v[192:195], v[64:67]
	v_mfma_f32_16x16x32_f16 v[56:59], v[156:159], v[188:191], v[56:59]
	v_mfma_f32_16x16x32_f16 v[56:59], v[160:163], v[192:195], v[56:59]
	v_mfma_f32_16x16x32_f16 v[48:51], v[148:151], v[176:179], v[48:51]
	v_mfma_f32_16x16x32_f16 v[48:51], v[152:155], v[180:183], v[48:51]
	v_mfma_f32_16x16x32_f16 v[40:43], v[156:159], v[176:179], v[40:43]
	v_mfma_f32_16x16x32_f16 v[40:43], v[160:163], v[180:183], v[40:43]
	v_mfma_f32_16x16x32_f16 v[32:35], v[148:151], v[172:175], v[32:35]
	v_mfma_f32_16x16x32_f16 v[32:35], v[152:155], v[184:187], v[32:35]
	v_mfma_f32_16x16x32_f16 v[24:27], v[156:159], v[172:175], v[24:27]
	v_mfma_f32_16x16x32_f16 v[24:27], v[160:163], v[184:187], v[24:27]
	v_mfma_f32_16x16x32_f16 v[16:19], v[148:151], v[164:167], v[16:19]
	v_mfma_f32_16x16x32_f16 v[16:19], v[152:155], v[168:171], v[16:19]
	v_mfma_f32_16x16x32_f16 v[8:11], v[156:159], v[164:167], v[8:11]
	v_mfma_f32_16x16x32_f16 v[8:11], v[160:163], v[168:171], v[8:11]
	s_setprio 0
	s_setprio 2
	v_mfma_f32_16x16x32_f16 v[60:63], v[132:135], v[188:191], v[60:63]
	v_mfma_f32_16x16x32_f16 v[60:63], v[136:139], v[192:195], v[60:63]
	v_mfma_f32_16x16x32_f16 v[52:55], v[140:143], v[188:191], v[52:55]
	v_mfma_f32_16x16x32_f16 v[52:55], v[144:147], v[192:195], v[52:55]
	v_mfma_f32_16x16x32_f16 v[44:47], v[132:135], v[176:179], v[44:47]
	v_mfma_f32_16x16x32_f16 v[44:47], v[136:139], v[180:183], v[44:47]
	v_mfma_f32_16x16x32_f16 v[36:39], v[140:143], v[176:179], v[36:39]
	v_mfma_f32_16x16x32_f16 v[36:39], v[144:147], v[180:183], v[36:39]
	v_mfma_f32_16x16x32_f16 v[28:31], v[132:135], v[172:175], v[28:31]
	v_mfma_f32_16x16x32_f16 v[28:31], v[136:139], v[184:187], v[28:31]
	v_mfma_f32_16x16x32_f16 v[20:23], v[140:143], v[172:175], v[20:23]
	v_mfma_f32_16x16x32_f16 v[20:23], v[144:147], v[184:187], v[20:23]
	v_mfma_f32_16x16x32_f16 v[12:15], v[132:135], v[164:167], v[12:15]
	v_mfma_f32_16x16x32_f16 v[12:15], v[136:139], v[168:171], v[12:15]
	v_mfma_f32_16x16x32_f16 v[4:7], v[140:143], v[164:167], v[4:7]
	v_mfma_f32_16x16x32_f16 v[4:7], v[144:147], v[168:171], v[4:7]
	s_setprio 0
	v_add_u32_e32 v132, s70, v222
	s_add_u32 s48, s48, 0x100000
	v_add_u32_e32 v133, s70, v223
	ds_read_b128 v[148:151], v132
	ds_read_b128 v[152:155], v133
	v_add_u32_e32 v132, s71, v222
	s_addc_u32 s49, s49, 0
	s_mov_b32 m0, s57
	v_add_u32_e32 v133, s71, v223
	ds_read_b128 v[156:159], v132
	ds_read_b128 v[160:163], v133
	v_add_u32_e32 v132, s72, v222
	v_add_u32_e32 v136, s72, v223
	v_add_u32_e32 v140, s73, v222
	v_add_u32_e32 v144, s73, v223
	v_lshl_add_u64 v[212:213], s[48:49], 0, v[202:203]
	ds_read_b128 v[132:135], v132
	ds_read_b128 v[136:139], v136
	ds_read_b128 v[140:143], v140
	ds_read_b128 v[144:147], v144
	ds_read_b128 v[188:191], v226 offset:32768
	ds_read_b128 v[176:179], v226 offset:34816
	ds_read_b128 v[192:195], v227 offset:32768
	ds_read_b128 v[180:183], v227 offset:34816
	ds_read_b128 v[172:175], v226 offset:36864
	ds_read_b128 v[164:167], v226 offset:38912
	ds_read_b128 v[184:187], v227 offset:36864
	ds_read_b128 v[168:171], v227 offset:38912
	global_load_lds_dwordx4 v[212:213], off
	v_lshl_add_u64 v[212:213], s[48:49], 0, v[198:199]
	s_mov_b32 m0, s58
	s_mov_b64 s[48:49], -1
	global_load_lds_dwordx4 v[212:213], off
	s_mov_b64 vcc, s[4:5]
	s_cbranch_vccz .Lk1y_22
	s_waitcnt vmcnt(8)
	s_mov_b64 s[48:49], 0

.Lk1y_24:
	s_waitcnt lgkmcnt(0)
	s_barrier
	s_setprio 2
	s_waitcnt lgkmcnt(0)
	v_mfma_f32_16x16x32_f16 v[128:131], v[148:151], v[188:191], v[128:131]
	v_mfma_f32_16x16x32_f16 v[128:131], v[152:155], v[192:195], v[128:131]
	v_mfma_f32_16x16x32_f16 v[120:123], v[156:159], v[188:191], v[120:123]
	v_mfma_f32_16x16x32_f16 v[120:123], v[160:163], v[192:195], v[120:123]
	v_mfma_f32_16x16x32_f16 v[112:115], v[148:151], v[176:179], v[112:115]
	v_mfma_f32_16x16x32_f16 v[112:115], v[152:155], v[180:183], v[112:115]
	v_mfma_f32_16x16x32_f16 v[104:107], v[156:159], v[176:179], v[104:107]
	v_mfma_f32_16x16x32_f16 v[104:107], v[160:163], v[180:183], v[104:107]
	v_mfma_f32_16x16x32_f16 v[96:99], v[148:151], v[172:175], v[96:99]
	v_mfma_f32_16x16x32_f16 v[96:99], v[152:155], v[184:187], v[96:99]
	v_mfma_f32_16x16x32_f16 v[88:91], v[156:159], v[172:175], v[88:91]
	v_mfma_f32_16x16x32_f16 v[88:91], v[160:163], v[184:187], v[88:91]
	v_mfma_f32_16x16x32_f16 v[80:83], v[148:151], v[164:167], v[80:83]
	v_mfma_f32_16x16x32_f16 v[80:83], v[152:155], v[168:171], v[80:83]
	v_mfma_f32_16x16x32_f16 v[72:75], v[156:159], v[164:167], v[72:75]
	v_mfma_f32_16x16x32_f16 v[72:75], v[160:163], v[168:171], v[72:75]
	s_setprio 0
	s_setprio 2
	v_mfma_f32_16x16x32_f16 v[124:127], v[132:135], v[188:191], v[124:127]
	v_mfma_f32_16x16x32_f16 v[124:127], v[136:139], v[192:195], v[124:127]
	v_mfma_f32_16x16x32_f16 v[116:119], v[140:143], v[188:191], v[116:119]
	v_mfma_f32_16x16x32_f16 v[116:119], v[144:147], v[192:195], v[116:119]
	v_mfma_f32_16x16x32_f16 v[108:111], v[132:135], v[176:179], v[108:111]
	v_mfma_f32_16x16x32_f16 v[108:111], v[136:139], v[180:183], v[108:111]
	v_mfma_f32_16x16x32_f16 v[100:103], v[140:143], v[176:179], v[100:103]
	v_mfma_f32_16x16x32_f16 v[100:103], v[144:147], v[180:183], v[100:103]
	v_mfma_f32_16x16x32_f16 v[92:95], v[132:135], v[172:175], v[92:95]
	v_mfma_f32_16x16x32_f16 v[92:95], v[136:139], v[184:187], v[92:95]
	v_mfma_f32_16x16x32_f16 v[84:87], v[140:143], v[172:175], v[84:87]
	v_mfma_f32_16x16x32_f16 v[84:87], v[144:147], v[184:187], v[84:87]
	v_mfma_f32_16x16x32_f16 v[76:79], v[132:135], v[164:167], v[76:79]
	v_mfma_f32_16x16x32_f16 v[76:79], v[136:139], v[168:171], v[76:79]
	v_mfma_f32_16x16x32_f16 v[68:71], v[140:143], v[164:167], v[68:71]
	v_mfma_f32_16x16x32_f16 v[68:71], v[144:147], v[168:171], v[68:71]
	s_setprio 0
	s_mov_b32 m0, s59
	v_lshl_add_u64 v[212:213], v[214:215], 0, s[24:25]
	s_add_u32 s4, s46, 0x100080
	ds_read_b128 v[164:167], v226 offset:49152
	ds_read_b128 v[168:171], v226 offset:51200
	ds_read_b128 v[172:175], v227 offset:49152
	ds_read_b128 v[176:179], v227 offset:51200
	ds_read_b128 v[180:183], v226 offset:53248
	ds_read_b128 v[184:187], v226 offset:55296
	ds_read_b128 v[188:191], v227 offset:53248
	ds_read_b128 v[192:195], v227 offset:55296
	global_load_lds_dwordx4 v[212:213], off
	v_lshl_add_u64 v[212:213], v[216:217], 0, s[24:25]
	s_mov_b32 m0, s60
	s_addc_u32 s5, s47, 0
	global_load_lds_dwordx4 v[212:213], off
	v_lshl_add_u64 v[212:213], s[4:5], 0, v[200:201]
	s_mov_b32 m0, s63
	s_nop 0
	global_load_lds_dwordx4 v[212:213], off
	v_lshl_add_u64 v[212:213], s[4:5], 0, v[196:197]
	s_mov_b32 m0, s64
	s_nop 0
	global_load_lds_dwordx4 v[212:213], off
	v_lshl_add_u64 v[212:213], v[218:219], 0, s[24:25]
	s_mov_b32 m0, s61
	s_nop 0
	global_load_lds_dwordx4 v[212:213], off
	v_lshl_add_u64 v[212:213], v[220:221], 0, s[24:25]
	s_mov_b32 m0, s62
	s_nop 0
	global_load_lds_dwordx4 v[212:213], off
	s_waitcnt vmcnt(8)
	s_waitcnt lgkmcnt(0)
	s_barrier
	s_setprio 2
	s_waitcnt lgkmcnt(0)
	v_mfma_f32_16x16x32_f16 v[64:67], v[148:151], v[164:167], v[64:67]
	v_mfma_f32_16x16x32_f16 v[64:67], v[152:155], v[172:175], v[64:67]
	v_mfma_f32_16x16x32_f16 v[56:59], v[156:159], v[164:167], v[56:59]
	v_mfma_f32_16x16x32_f16 v[56:59], v[160:163], v[172:175], v[56:59]
	v_mfma_f32_16x16x32_f16 v[48:51], v[148:151], v[168:171], v[48:51]
	v_mfma_f32_16x16x32_f16 v[48:51], v[152:155], v[176:179], v[48:51]
	v_mfma_f32_16x16x32_f16 v[40:43], v[156:159], v[168:171], v[40:43]
	v_mfma_f32_16x16x32_f16 v[40:43], v[160:163], v[176:179], v[40:43]
	v_mfma_f32_16x16x32_f16 v[32:35], v[148:151], v[180:183], v[32:35]
	v_mfma_f32_16x16x32_f16 v[32:35], v[152:155], v[188:191], v[32:35]
	v_mfma_f32_16x16x32_f16 v[24:27], v[156:159], v[180:183], v[24:27]
	v_mfma_f32_16x16x32_f16 v[24:27], v[160:163], v[188:191], v[24:27]
	v_mfma_f32_16x16x32_f16 v[16:19], v[148:151], v[184:187], v[16:19]
	v_mfma_f32_16x16x32_f16 v[16:19], v[152:155], v[192:195], v[16:19]
	v_mfma_f32_16x16x32_f16 v[8:11], v[156:159], v[184:187], v[8:11]
	v_mfma_f32_16x16x32_f16 v[8:11], v[160:163], v[192:195], v[8:11]
	s_setprio 0
	s_setprio 2
	v_mfma_f32_16x16x32_f16 v[60:63], v[132:135], v[164:167], v[60:63]
	v_mfma_f32_16x16x32_f16 v[60:63], v[136:139], v[172:175], v[60:63]
	v_mfma_f32_16x16x32_f16 v[52:55], v[140:143], v[164:167], v[52:55]
	v_mfma_f32_16x16x32_f16 v[52:55], v[144:147], v[172:175], v[52:55]
	v_mfma_f32_16x16x32_f16 v[44:47], v[132:135], v[168:171], v[44:47]
	v_mfma_f32_16x16x32_f16 v[44:47], v[136:139], v[176:179], v[44:47]
	v_mfma_f32_16x16x32_f16 v[36:39], v[140:143], v[168:171], v[36:39]
	v_mfma_f32_16x16x32_f16 v[36:39], v[144:147], v[176:179], v[36:39]
	v_mfma_f32_16x16x32_f16 v[28:31], v[132:135], v[180:183], v[28:31]
	v_mfma_f32_16x16x32_f16 v[28:31], v[136:139], v[188:191], v[28:31]
	v_mfma_f32_16x16x32_f16 v[20:23], v[140:143], v[180:183], v[20:23]
	v_mfma_f32_16x16x32_f16 v[20:23], v[144:147], v[188:191], v[20:23]
	v_mfma_f32_16x16x32_f16 v[12:15], v[132:135], v[184:187], v[12:15]
	v_mfma_f32_16x16x32_f16 v[12:15], v[136:139], v[192:195], v[12:15]
	v_mfma_f32_16x16x32_f16 v[4:7], v[140:143], v[184:187], v[4:7]
	v_mfma_f32_16x16x32_f16 v[4:7], v[144:147], v[192:195], v[4:7]
	s_setprio 0
	s_add_u32 s80, s80, 0x100
	s_addc_u32 s81, s81, 0
	s_add_u32 s44, s44, 0x100
	s_addc_u32 s45, s45, 0
	s_cmp_gt_u32 s82, 61
	s_cbranch_scc1 .LBB1_4
	s_mov_b32 s48, s82
	s_branch .Lk1y_9

.LBB1_27:
	s_waitcnt vmcnt(0)
	s_barrier
.LBB1_30:
	s_endpgm
	s_nop 0
	s_nop 0
	s_nop 0
	s_nop 0
	s_nop 0
	s_nop 0
	s_nop 0
	s_nop 0
	s_nop 0
	s_nop 0
	s_nop 0
	s_nop 0
	s_nop 0
	s_nop 0
	s_nop 0
	s_nop 0
	s_nop 0
	s_nop 0
	s_nop 0
	s_nop 0
	s_nop 0
	s_nop 0
	s_nop 0
	s_nop 0
	s_nop 0
	s_nop 0
	s_nop 0
	s_nop 0
	s_nop 0
	s_nop 0
	s_nop 0
	s_nop 0
	s_nop 0
	s_nop 0
	s_nop 0
	s_nop 0
	s_nop 0
	s_nop 0
	s_nop 0
	s_nop 0
	s_nop 0
	s_nop 0
	s_endpgm

.Lk2_loopX:
	s_add_u32 s30, s28, 0xffc80080
	s_addc_u32 s31, s29, -1
	s_cmpk_eq_i32 s58, 0xdc
	s_cselect_b32 s35, s25, s31
	s_cselect_b32 s34, s24, s30
	s_cselect_b32 s31, s27, s57
	s_cselect_b32 s30, s26, s56
	v_lshl_add_u64 v[138:139], s[28:29], 0, v[134:135]
	s_add_i32 m0, s37, 0xc000
	ds_read_b128 v[166:169], v143
	ds_read_b128 v[170:173], v147
	ds_read_b128 v[174:177], v149
	ds_read_b128 v[178:181], v150
	ds_read_b128 v[182:185], v151
	ds_read_b128 v[186:189], v152
	ds_read_b128 v[190:193], v153
	ds_read_b128 v[194:197], v154
	ds_read_b128 v[198:201], v155
	ds_read_b128 v[202:205], v155 offset:2048
	ds_read_b128 v[206:209], v156
	ds_read_b128 v[210:213], v156 offset:2048
	ds_read_b128 v[214:217], v155 offset:4096
	ds_read_b128 v[218:221], v155 offset:6144
	ds_read_b128 v[222:225], v156 offset:4096
	ds_read_b128 v[226:229], v156 offset:6144
	global_load_lds_dwordx4 v[138:139], off
	v_lshl_add_u64 v[138:139], s[28:29], 0, v[132:133]
	s_add_i32 m0, s37, 0xe000
	s_nop 0
	global_load_lds_dwordx4 v[138:139], off
	s_waitcnt vmcnt(8)
	s_waitcnt lgkmcnt(0)
	s_setprio 1
	s_waitcnt lgkmcnt(0)
	v_mfma_f32_16x16x32_f16 v[124:127], v[166:169], v[198:201], v[124:127]
	v_mfma_f32_16x16x32_f16 v[124:127], v[170:173], v[206:209], v[124:127]
	v_mfma_f32_16x16x32_f16 v[120:123], v[174:177], v[198:201], v[120:123]
	v_mfma_f32_16x16x32_f16 v[120:123], v[178:181], v[206:209], v[120:123]
	v_mfma_f32_16x16x32_f16 v[116:119], v[166:169], v[202:205], v[116:119]
	v_mfma_f32_16x16x32_f16 v[116:119], v[170:173], v[210:213], v[116:119]
	v_mfma_f32_16x16x32_f16 v[112:115], v[174:177], v[202:205], v[112:115]
	v_mfma_f32_16x16x32_f16 v[112:115], v[178:181], v[210:213], v[112:115]
	v_mfma_f32_16x16x32_f16 v[108:111], v[166:169], v[214:217], v[108:111]
	v_mfma_f32_16x16x32_f16 v[108:111], v[170:173], v[222:225], v[108:111]
	v_mfma_f32_16x16x32_f16 v[100:103], v[174:177], v[214:217], v[100:103]
	v_mfma_f32_16x16x32_f16 v[100:103], v[178:181], v[222:225], v[100:103]
	v_mfma_f32_16x16x32_f16 v[92:95], v[166:169], v[218:221], v[92:95]
	v_mfma_f32_16x16x32_f16 v[92:95], v[170:173], v[226:229], v[92:95]
	v_mfma_f32_16x16x32_f16 v[84:87], v[174:177], v[218:221], v[84:87]
	v_mfma_f32_16x16x32_f16 v[84:87], v[178:181], v[226:229], v[84:87]
	s_setprio 0
	s_setprio 1
	v_mfma_f32_16x16x32_f16 v[104:107], v[182:185], v[198:201], v[104:107]
	v_mfma_f32_16x16x32_f16 v[104:107], v[186:189], v[206:209], v[104:107]
	v_mfma_f32_16x16x32_f16 v[96:99], v[190:193], v[198:201], v[96:99]
	v_mfma_f32_16x16x32_f16 v[96:99], v[194:197], v[206:209], v[96:99]
	v_mfma_f32_16x16x32_f16 v[88:91], v[182:185], v[202:205], v[88:91]
	v_mfma_f32_16x16x32_f16 v[88:91], v[186:189], v[210:213], v[88:91]
	v_mfma_f32_16x16x32_f16 v[80:83], v[190:193], v[202:205], v[80:83]
	v_mfma_f32_16x16x32_f16 v[80:83], v[194:197], v[210:213], v[80:83]
	v_mfma_f32_16x16x32_f16 v[76:79], v[182:185], v[214:217], v[76:79]
	v_mfma_f32_16x16x32_f16 v[76:79], v[186:189], v[222:225], v[76:79]
	v_mfma_f32_16x16x32_f16 v[72:75], v[190:193], v[214:217], v[72:75]
	v_mfma_f32_16x16x32_f16 v[72:75], v[194:197], v[222:225], v[72:75]
	v_mfma_f32_16x16x32_f16 v[68:71], v[182:185], v[218:221], v[68:71]
	v_mfma_f32_16x16x32_f16 v[68:71], v[186:189], v[226:229], v[68:71]
	v_mfma_f32_16x16x32_f16 v[64:67], v[190:193], v[218:221], v[64:67]
	v_mfma_f32_16x16x32_f16 v[64:67], v[194:197], v[226:229], v[64:67]
	s_setprio 0
	s_barrier
	s_add_i32 s59, s43, s36
	v_lshl_add_u64 v[138:139], s[30:31], 0, v[128:129]
	s_mov_b32 m0, s59
	ds_read_b128 v[198:201], v155 offset:16384
	ds_read_b128 v[202:205], v155 offset:18432
	ds_read_b128 v[206:209], v156 offset:16384
	ds_read_b128 v[210:213], v156 offset:18432
	ds_read_b128 v[214:217], v155 offset:20480
	ds_read_b128 v[218:221], v155 offset:22528
	ds_read_b128 v[222:225], v156 offset:20480
	ds_read_b128 v[226:229], v156 offset:22528
	global_load_lds_dwordx4 v[138:139], off
	s_add_i32 m0, s59, 0x2000
	s_add_u32 s60, s30, 0x380000
	v_lshl_add_u64 v[144:145], s[30:31], 0, v[130:131]
	s_addc_u32 s61, s31, 0
	s_add_i32 s59, s44, s36
	global_load_lds_dwordx4 v[144:145], off
	v_lshl_add_u64 v[230:231], s[60:61], 0, v[128:129]
	s_mov_b32 m0, s59
	v_lshl_add_u64 v[232:233], s[34:35], 0, v[130:131]
	global_load_lds_dwordx4 v[230:231], off
	v_lshl_add_u64 v[230:231], s[60:61], 0, v[130:131]
	s_add_i32 m0, s59, 0x2000
	s_nop 0
	global_load_lds_dwordx4 v[230:231], off
	v_lshl_add_u64 v[230:231], s[34:35], 0, v[128:129]
	s_mov_b32 m0, s37
	s_nop 0
	global_load_lds_dwordx4 v[230:231], off
	s_mov_b32 m0, s38
	s_nop 0
	global_load_lds_dwordx4 v[232:233], off
	s_waitcnt vmcnt(8)
	s_waitcnt lgkmcnt(0)
	s_setprio 1
	s_waitcnt lgkmcnt(0)
	v_mfma_f32_16x16x32_f16 v[60:63], v[166:169], v[198:201], v[60:63]
	v_mfma_f32_16x16x32_f16 v[60:63], v[170:173], v[206:209], v[60:63]
	v_mfma_f32_16x16x32_f16 v[56:59], v[174:177], v[198:201], v[56:59]
	v_mfma_f32_16x16x32_f16 v[56:59], v[178:181], v[206:209], v[56:59]
	v_mfma_f32_16x16x32_f16 v[52:55], v[166:169], v[202:205], v[52:55]
	v_mfma_f32_16x16x32_f16 v[52:55], v[170:173], v[210:213], v[52:55]
	v_mfma_f32_16x16x32_f16 v[48:51], v[174:177], v[202:205], v[48:51]
	v_mfma_f32_16x16x32_f16 v[48:51], v[178:181], v[210:213], v[48:51]
	v_mfma_f32_16x16x32_f16 v[40:43], v[166:169], v[214:217], v[40:43]
	v_mfma_f32_16x16x32_f16 v[40:43], v[170:173], v[222:225], v[40:43]
	v_mfma_f32_16x16x32_f16 v[32:35], v[174:177], v[214:217], v[32:35]
	v_mfma_f32_16x16x32_f16 v[32:35], v[178:181], v[222:225], v[32:35]
	v_mfma_f32_16x16x32_f16 v[12:15], v[166:169], v[218:221], v[12:15]
	v_mfma_f32_16x16x32_f16 v[12:15], v[170:173], v[226:229], v[12:15]
	v_mfma_f32_16x16x32_f16 v[8:11], v[174:177], v[218:221], v[8:11]
	v_mfma_f32_16x16x32_f16 v[8:11], v[178:181], v[226:229], v[8:11]
	s_setprio 0
	s_setprio 1
	v_mfma_f32_16x16x32_f16 v[44:47], v[182:185], v[198:201], v[44:47]
	v_mfma_f32_16x16x32_f16 v[44:47], v[186:189], v[206:209], v[44:47]
	v_mfma_f32_16x16x32_f16 v[36:39], v[190:193], v[198:201], v[36:39]
	v_mfma_f32_16x16x32_f16 v[36:39], v[194:197], v[206:209], v[36:39]
	v_mfma_f32_16x16x32_f16 v[28:31], v[182:185], v[202:205], v[28:31]
	v_mfma_f32_16x16x32_f16 v[28:31], v[186:189], v[210:213], v[28:31]
	v_mfma_f32_16x16x32_f16 v[24:27], v[190:193], v[202:205], v[24:27]
	v_mfma_f32_16x16x32_f16 v[24:27], v[194:197], v[210:213], v[24:27]
	v_mfma_f32_16x16x32_f16 v[20:23], v[182:185], v[214:217], v[20:23]
	v_mfma_f32_16x16x32_f16 v[20:23], v[186:189], v[222:225], v[20:23]
	v_mfma_f32_16x16x32_f16 v[16:19], v[190:193], v[214:217], v[16:19]
	v_mfma_f32_16x16x32_f16 v[16:19], v[194:197], v[222:225], v[16:19]
	v_mfma_f32_16x16x32_f16 v[4:7], v[182:185], v[218:221], v[4:7]
	v_mfma_f32_16x16x32_f16 v[4:7], v[186:189], v[226:229], v[4:7]
	v_mfma_f32_16x16x32_f16 v[0:3], v[190:193], v[218:221], v[0:3]
	v_mfma_f32_16x16x32_f16 v[0:3], v[194:197], v[226:229], v[0:3]
	s_setprio 0
	s_barrier
	s_add_u32 s34, s34, 0x380000
	s_addc_u32 s35, s35, 0
	s_mov_b32 m0, s39
	v_lshl_add_u64 v[234:235], s[34:35], 0, v[128:129]
	ds_read_b128 v[166:169], v157
	ds_read_b128 v[170:173], v158
	ds_read_b128 v[174:177], v159
	ds_read_b128 v[178:181], v160
	ds_read_b128 v[182:185], v161
	ds_read_b128 v[186:189], v162
	ds_read_b128 v[190:193], v163
	ds_read_b128 v[194:197], v164
	ds_read_b128 v[198:201], v155 offset:32768
	ds_read_b128 v[202:205], v155 offset:34816
	ds_read_b128 v[206:209], v156 offset:32768
	ds_read_b128 v[210:213], v156 offset:34816
	ds_read_b128 v[214:217], v155 offset:36864
	ds_read_b128 v[218:221], v155 offset:38912
	ds_read_b128 v[222:225], v156 offset:36864
	ds_read_b128 v[226:229], v156 offset:38912
	global_load_lds_dwordx4 v[234:235], off
	v_lshl_add_u64 v[234:235], s[34:35], 0, v[130:131]
	s_mov_b32 m0, s40
	s_nop 0
	global_load_lds_dwordx4 v[234:235], off
	s_waitcnt vmcnt(8)
	s_waitcnt lgkmcnt(0)
	s_setprio 1
	s_waitcnt lgkmcnt(0)
	v_mfma_f32_16x16x32_f16 v[124:127], v[166:169], v[198:201], v[124:127]
	v_mfma_f32_16x16x32_f16 v[124:127], v[170:173], v[206:209], v[124:127]
	v_mfma_f32_16x16x32_f16 v[120:123], v[174:177], v[198:201], v[120:123]
	v_mfma_f32_16x16x32_f16 v[120:123], v[178:181], v[206:209], v[120:123]
	v_mfma_f32_16x16x32_f16 v[116:119], v[166:169], v[202:205], v[116:119]
	v_mfma_f32_16x16x32_f16 v[116:119], v[170:173], v[210:213], v[116:119]
	v_mfma_f32_16x16x32_f16 v[112:115], v[174:177], v[202:205], v[112:115]
	v_mfma_f32_16x16x32_f16 v[112:115], v[178:181], v[210:213], v[112:115]
	v_mfma_f32_16x16x32_f16 v[108:111], v[166:169], v[214:217], v[108:111]
	v_mfma_f32_16x16x32_f16 v[108:111], v[170:173], v[222:225], v[108:111]
	v_mfma_f32_16x16x32_f16 v[100:103], v[174:177], v[214:217], v[100:103]
	v_mfma_f32_16x16x32_f16 v[100:103], v[178:181], v[222:225], v[100:103]
	v_mfma_f32_16x16x32_f16 v[92:95], v[166:169], v[218:221], v[92:95]
	v_mfma_f32_16x16x32_f16 v[92:95], v[170:173], v[226:229], v[92:95]
	v_mfma_f32_16x16x32_f16 v[84:87], v[174:177], v[218:221], v[84:87]
	v_mfma_f32_16x16x32_f16 v[84:87], v[178:181], v[226:229], v[84:87]
	s_setprio 0
	s_setprio 1
	v_mfma_f32_16x16x32_f16 v[104:107], v[182:185], v[198:201], v[104:107]
	v_mfma_f32_16x16x32_f16 v[104:107], v[186:189], v[206:209], v[104:107]
	v_mfma_f32_16x16x32_f16 v[96:99], v[190:193], v[198:201], v[96:99]
	v_mfma_f32_16x16x32_f16 v[96:99], v[194:197], v[206:209], v[96:99]
	v_mfma_f32_16x16x32_f16 v[88:91], v[182:185], v[202:205], v[88:91]
	v_mfma_f32_16x16x32_f16 v[88:91], v[186:189], v[210:213], v[88:91]
	v_mfma_f32_16x16x32_f16 v[80:83], v[190:193], v[202:205], v[80:83]
	v_mfma_f32_16x16x32_f16 v[80:83], v[194:197], v[210:213], v[80:83]
	v_mfma_f32_16x16x32_f16 v[76:79], v[182:185], v[214:217], v[76:79]
	v_mfma_f32_16x16x32_f16 v[76:79], v[186:189], v[222:225], v[76:79]
	v_mfma_f32_16x16x32_f16 v[72:75], v[190:193], v[214:217], v[72:75]
	v_mfma_f32_16x16x32_f16 v[72:75], v[194:197], v[222:225], v[72:75]
	v_mfma_f32_16x16x32_f16 v[68:71], v[182:185], v[218:221], v[68:71]
	v_mfma_f32_16x16x32_f16 v[68:71], v[186:189], v[226:229], v[68:71]
	v_mfma_f32_16x16x32_f16 v[64:67], v[190:193], v[218:221], v[64:67]
	v_mfma_f32_16x16x32_f16 v[64:67], v[194:197], v[226:229], v[64:67]
	s_setprio 0
	s_barrier
	s_add_i32 s34, s46, s36
	v_lshl_add_u64 v[138:139], v[138:139], 0, s[14:15]
	s_mov_b32 m0, s34
	ds_read_b128 v[198:201], v155 offset:49152
	ds_read_b128 v[202:205], v155 offset:51200
	ds_read_b128 v[206:209], v156 offset:49152
	ds_read_b128 v[210:213], v156 offset:51200
	ds_read_b128 v[214:217], v155 offset:53248
	ds_read_b128 v[218:221], v155 offset:55296
	ds_read_b128 v[222:225], v156 offset:53248
	ds_read_b128 v[226:229], v156 offset:55296
	global_load_lds_dwordx4 v[138:139], off
	s_add_i32 m0, s34, 0x2000
	s_add_u32 s30, s30, 0x380080
	v_lshl_add_u64 v[138:139], v[144:145], 0, s[14:15]
	s_addc_u32 s31, s31, 0
	s_add_i32 s34, s47, s36
	global_load_lds_dwordx4 v[138:139], off
	v_lshl_add_u64 v[138:139], s[30:31], 0, v[128:129]
	s_mov_b32 m0, s34
	s_nop 0
	global_load_lds_dwordx4 v[138:139], off
	v_lshl_add_u64 v[138:139], s[30:31], 0, v[130:131]
	s_add_i32 m0, s34, 0x2000
	s_nop 0
	global_load_lds_dwordx4 v[138:139], off
	v_lshl_add_u64 v[138:139], v[230:231], 0, s[14:15]
	s_mov_b32 m0, s41
	s_nop 0
	global_load_lds_dwordx4 v[138:139], off
	v_lshl_add_u64 v[138:139], v[232:233], 0, s[14:15]
	s_mov_b32 m0, s42
	s_nop 0
	global_load_lds_dwordx4 v[138:139], off
	s_waitcnt vmcnt(8)
	s_waitcnt lgkmcnt(0)
	s_setprio 1
	s_waitcnt lgkmcnt(0)
	v_mfma_f32_16x16x32_f16 v[60:63], v[166:169], v[198:201], v[60:63]
	v_mfma_f32_16x16x32_f16 v[60:63], v[170:173], v[206:209], v[60:63]
	v_mfma_f32_16x16x32_f16 v[56:59], v[174:177], v[198:201], v[56:59]
	v_mfma_f32_16x16x32_f16 v[56:59], v[178:181], v[206:209], v[56:59]
	v_mfma_f32_16x16x32_f16 v[52:55], v[166:169], v[202:205], v[52:55]
	v_mfma_f32_16x16x32_f16 v[52:55], v[170:173], v[210:213], v[52:55]
	v_mfma_f32_16x16x32_f16 v[48:51], v[174:177], v[202:205], v[48:51]
	v_mfma_f32_16x16x32_f16 v[48:51], v[178:181], v[210:213], v[48:51]
	v_mfma_f32_16x16x32_f16 v[40:43], v[166:169], v[214:217], v[40:43]
	v_mfma_f32_16x16x32_f16 v[40:43], v[170:173], v[222:225], v[40:43]
	v_mfma_f32_16x16x32_f16 v[32:35], v[174:177], v[214:217], v[32:35]
	v_mfma_f32_16x16x32_f16 v[32:35], v[178:181], v[222:225], v[32:35]
	v_mfma_f32_16x16x32_f16 v[12:15], v[166:169], v[218:221], v[12:15]
	v_mfma_f32_16x16x32_f16 v[12:15], v[170:173], v[226:229], v[12:15]
	v_mfma_f32_16x16x32_f16 v[8:11], v[174:177], v[218:221], v[8:11]
	v_mfma_f32_16x16x32_f16 v[8:11], v[178:181], v[226:229], v[8:11]
	s_setprio 0
	s_setprio 1
	v_mfma_f32_16x16x32_f16 v[44:47], v[182:185], v[198:201], v[44:47]
	v_mfma_f32_16x16x32_f16 v[44:47], v[186:189], v[206:209], v[44:47]
	v_mfma_f32_16x16x32_f16 v[36:39], v[190:193], v[198:201], v[36:39]
	v_mfma_f32_16x16x32_f16 v[36:39], v[194:197], v[206:209], v[36:39]
	v_mfma_f32_16x16x32_f16 v[28:31], v[182:185], v[202:205], v[28:31]
	v_mfma_f32_16x16x32_f16 v[28:31], v[186:189], v[210:213], v[28:31]
	v_mfma_f32_16x16x32_f16 v[24:27], v[190:193], v[202:205], v[24:27]
	v_mfma_f32_16x16x32_f16 v[24:27], v[194:197], v[210:213], v[24:27]
	v_mfma_f32_16x16x32_f16 v[20:23], v[182:185], v[214:217], v[20:23]
	v_mfma_f32_16x16x32_f16 v[20:23], v[186:189], v[222:225], v[20:23]
	v_mfma_f32_16x16x32_f16 v[16:19], v[190:193], v[214:217], v[16:19]
	v_mfma_f32_16x16x32_f16 v[16:19], v[194:197], v[222:225], v[16:19]
	v_mfma_f32_16x16x32_f16 v[4:7], v[182:185], v[218:221], v[4:7]
	v_mfma_f32_16x16x32_f16 v[4:7], v[186:189], v[226:229], v[4:7]
	v_mfma_f32_16x16x32_f16 v[0:3], v[190:193], v[218:221], v[0:3]
	v_mfma_f32_16x16x32_f16 v[0:3], v[194:197], v[226:229], v[0:3]
	s_setprio 0
	s_barrier
	s_add_i32 s58, s58, 2
	s_add_u32 s56, s56, 0x100
	s_addc_u32 s57, s57, 0
	s_add_u32 s28, s28, 0x100
	s_addc_u32 s29, s29, 0
	s_cmpk_gt_u32 s58, 0xdd
	s_cbranch_scc0 .Lk2_loopX
	s_branch .Lk2_epi
	s_nop 0
	s_nop 0
	s_nop 0
	s_nop 0
	s_nop 0
	s_nop 0
	s_nop 0
	s_nop 0
	s_nop 0
.Lk2_loopY:
	s_add_u32 s30, s28, 0xffc80080
	s_addc_u32 s31, s29, -1
	s_cmpk_eq_i32 s58, 0xdc
	s_cselect_b32 s35, s25, s31
	s_cselect_b32 s34, s24, s30
	s_cselect_b32 s31, s27, s57
	s_cselect_b32 s30, s26, s56
	v_lshl_add_u64 v[138:139], s[28:29], 0, v[134:135]
	s_add_i32 m0, s37, 0xc000
	ds_read_b128 v[166:169], v143
	ds_read_b128 v[170:173], v147
	ds_read_b128 v[174:177], v149
	ds_read_b128 v[178:181], v150
	ds_read_b128 v[182:185], v151
	ds_read_b128 v[186:189], v152
	ds_read_b128 v[190:193], v153
	ds_read_b128 v[194:197], v154
	ds_read_b128 v[198:201], v155
	ds_read_b128 v[202:205], v155 offset:2048
	ds_read_b128 v[206:209], v156
	ds_read_b128 v[210:213], v156 offset:2048
	ds_read_b128 v[214:217], v155 offset:4096
	ds_read_b128 v[218:221], v155 offset:6144
	ds_read_b128 v[222:225], v156 offset:4096
	ds_read_b128 v[226:229], v156 offset:6144
	global_load_lds_dwordx4 v[138:139], off
	v_lshl_add_u64 v[138:139], s[28:29], 0, v[132:133]
	s_add_i32 m0, s37, 0xe000
	s_nop 0
	global_load_lds_dwordx4 v[138:139], off
	s_waitcnt vmcnt(8)
	s_waitcnt lgkmcnt(0)
	s_barrier
	s_setprio 2
	s_waitcnt lgkmcnt(0)
	v_mfma_f32_16x16x32_f16 v[124:127], v[166:169], v[198:201], v[124:127]
	v_mfma_f32_16x16x32_f16 v[124:127], v[170:173], v[206:209], v[124:127]
	v_mfma_f32_16x16x32_f16 v[120:123], v[174:177], v[198:201], v[120:123]
	v_mfma_f32_16x16x32_f16 v[120:123], v[178:181], v[206:209], v[120:123]
	v_mfma_f32_16x16x32_f16 v[116:119], v[166:169], v[202:205], v[116:119]
	v_mfma_f32_16x16x32_f16 v[116:119], v[170:173], v[210:213], v[116:119]
	v_mfma_f32_16x16x32_f16 v[112:115], v[174:177], v[202:205], v[112:115]
	v_mfma_f32_16x16x32_f16 v[112:115], v[178:181], v[210:213], v[112:115]
	v_mfma_f32_16x16x32_f16 v[108:111], v[166:169], v[214:217], v[108:111]
	v_mfma_f32_16x16x32_f16 v[108:111], v[170:173], v[222:225], v[108:111]
	v_mfma_f32_16x16x32_f16 v[100:103], v[174:177], v[214:217], v[100:103]
	v_mfma_f32_16x16x32_f16 v[100:103], v[178:181], v[222:225], v[100:103]
	v_mfma_f32_16x16x32_f16 v[92:95], v[166:169], v[218:221], v[92:95]
	v_mfma_f32_16x16x32_f16 v[92:95], v[170:173], v[226:229], v[92:95]
	v_mfma_f32_16x16x32_f16 v[84:87], v[174:177], v[218:221], v[84:87]
	v_mfma_f32_16x16x32_f16 v[84:87], v[178:181], v[226:229], v[84:87]
	s_setprio 0
	s_setprio 2
	v_mfma_f32_16x16x32_f16 v[104:107], v[182:185], v[198:201], v[104:107]
	v_mfma_f32_16x16x32_f16 v[104:107], v[186:189], v[206:209], v[104:107]
	v_mfma_f32_16x16x32_f16 v[96:99], v[190:193], v[198:201], v[96:99]
	v_mfma_f32_16x16x32_f16 v[96:99], v[194:197], v[206:209], v[96:99]
	v_mfma_f32_16x16x32_f16 v[88:91], v[182:185], v[202:205], v[88:91]
	v_mfma_f32_16x16x32_f16 v[88:91], v[186:189], v[210:213], v[88:91]
	v_mfma_f32_16x16x32_f16 v[80:83], v[190:193], v[202:205], v[80:83]
	v_mfma_f32_16x16x32_f16 v[80:83], v[194:197], v[210:213], v[80:83]
	v_mfma_f32_16x16x32_f16 v[76:79], v[182:185], v[214:217], v[76:79]
	v_mfma_f32_16x16x32_f16 v[76:79], v[186:189], v[222:225], v[76:79]
	v_mfma_f32_16x16x32_f16 v[72:75], v[190:193], v[214:217], v[72:75]
	v_mfma_f32_16x16x32_f16 v[72:75], v[194:197], v[222:225], v[72:75]
	v_mfma_f32_16x16x32_f16 v[68:71], v[182:185], v[218:221], v[68:71]
	v_mfma_f32_16x16x32_f16 v[68:71], v[186:189], v[226:229], v[68:71]
	v_mfma_f32_16x16x32_f16 v[64:67], v[190:193], v[218:221], v[64:67]
	v_mfma_f32_16x16x32_f16 v[64:67], v[194:197], v[226:229], v[64:67]
	s_setprio 0
	s_add_i32 s59, s43, s36
	v_lshl_add_u64 v[138:139], s[30:31], 0, v[128:129]
	s_mov_b32 m0, s59
	ds_read_b128 v[198:201], v155 offset:16384
	ds_read_b128 v[202:205], v155 offset:18432
	ds_read_b128 v[206:209], v156 offset:16384
	ds_read_b128 v[210:213], v156 offset:18432
	ds_read_b128 v[214:217], v155 offset:20480
	ds_read_b128 v[218:221], v155 offset:22528
	ds_read_b128 v[222:225], v156 offset:20480
	ds_read_b128 v[226:229], v156 offset:22528
	global_load_lds_dwordx4 v[138:139], off
	s_add_i32 m0, s59, 0x2000
	s_add_u32 s60, s30, 0x380000
	v_lshl_add_u64 v[144:145], s[30:31], 0, v[130:131]
	s_addc_u32 s61, s31, 0
	s_add_i32 s59, s44, s36
	global_load_lds_dwordx4 v[144:145], off
	v_lshl_add_u64 v[230:231], s[60:61], 0, v[128:129]
	s_mov_b32 m0, s59
	v_lshl_add_u64 v[232:233], s[34:35], 0, v[130:131]
	global_load_lds_dwordx4 v[230:231], off
	v_lshl_add_u64 v[230:231], s[60:61], 0, v[130:131]
	s_add_i32 m0, s59, 0x2000
	s_nop 0
	global_load_lds_dwordx4 v[230:231], off
	v_lshl_add_u64 v[230:231], s[34:35], 0, v[128:129]
	s_mov_b32 m0, s37
	s_nop 0
	global_load_lds_dwordx4 v[230:231], off
	s_mov_b32 m0, s38
	s_nop 0
	global_load_lds_dwordx4 v[232:233], off
	s_waitcnt vmcnt(8)
	s_waitcnt lgkmcnt(0)
	s_barrier
	s_setprio 2
	s_waitcnt lgkmcnt(0)
	v_mfma_f32_16x16x32_f16 v[60:63], v[166:169], v[198:201], v[60:63]
	v_mfma_f32_16x16x32_f16 v[60:63], v[170:173], v[206:209], v[60:63]
	v_mfma_f32_16x16x32_f16 v[56:59], v[174:177], v[198:201], v[56:59]
	v_mfma_f32_16x16x32_f16 v[56:59], v[178:181], v[206:209], v[56:59]
	v_mfma_f32_16x16x32_f16 v[52:55], v[166:169], v[202:205], v[52:55]
	v_mfma_f32_16x16x32_f16 v[52:55], v[170:173], v[210:213], v[52:55]
	v_mfma_f32_16x16x32_f16 v[48:51], v[174:177], v[202:205], v[48:51]
	v_mfma_f32_16x16x32_f16 v[48:51], v[178:181], v[210:213], v[48:51]
	v_mfma_f32_16x16x32_f16 v[40:43], v[166:169], v[214:217], v[40:43]
	v_mfma_f32_16x16x32_f16 v[40:43], v[170:173], v[222:225], v[40:43]
	v_mfma_f32_16x16x32_f16 v[32:35], v[174:177], v[214:217], v[32:35]
	v_mfma_f32_16x16x32_f16 v[32:35], v[178:181], v[222:225], v[32:35]
	v_mfma_f32_16x16x32_f16 v[12:15], v[166:169], v[218:221], v[12:15]
	v_mfma_f32_16x16x32_f16 v[12:15], v[170:173], v[226:229], v[12:15]
	v_mfma_f32_16x16x32_f16 v[8:11], v[174:177], v[218:221], v[8:11]
	v_mfma_f32_16x16x32_f16 v[8:11], v[178:181], v[226:229], v[8:11]
	s_setprio 0
	s_setprio 2
	v_mfma_f32_16x16x32_f16 v[44:47], v[182:185], v[198:201], v[44:47]
	v_mfma_f32_16x16x32_f16 v[44:47], v[186:189], v[206:209], v[44:47]
	v_mfma_f32_16x16x32_f16 v[36:39], v[190:193], v[198:201], v[36:39]
	v_mfma_f32_16x16x32_f16 v[36:39], v[194:197], v[206:209], v[36:39]
	v_mfma_f32_16x16x32_f16 v[28:31], v[182:185], v[202:205], v[28:31]
	v_mfma_f32_16x16x32_f16 v[28:31], v[186:189], v[210:213], v[28:31]
	v_mfma_f32_16x16x32_f16 v[24:27], v[190:193], v[202:205], v[24:27]
	v_mfma_f32_16x16x32_f16 v[24:27], v[194:197], v[210:213], v[24:27]
	v_mfma_f32_16x16x32_f16 v[20:23], v[182:185], v[214:217], v[20:23]
	v_mfma_f32_16x16x32_f16 v[20:23], v[186:189], v[222:225], v[20:23]
	v_mfma_f32_16x16x32_f16 v[16:19], v[190:193], v[214:217], v[16:19]
	v_mfma_f32_16x16x32_f16 v[16:19], v[194:197], v[222:225], v[16:19]
	v_mfma_f32_16x16x32_f16 v[4:7], v[182:185], v[218:221], v[4:7]
	v_mfma_f32_16x16x32_f16 v[4:7], v[186:189], v[226:229], v[4:7]
	v_mfma_f32_16x16x32_f16 v[0:3], v[190:193], v[218:221], v[0:3]
	v_mfma_f32_16x16x32_f16 v[0:3], v[194:197], v[226:229], v[0:3]
	s_setprio 0
	s_add_u32 s34, s34, 0x380000
	s_addc_u32 s35, s35, 0
	s_mov_b32 m0, s39
	v_lshl_add_u64 v[234:235], s[34:35], 0, v[128:129]
	ds_read_b128 v[166:169], v157
	ds_read_b128 v[170:173], v158
	ds_read_b128 v[174:177], v159
	ds_read_b128 v[178:181], v160
	ds_read_b128 v[182:185], v161
	ds_read_b128 v[186:189], v162
	ds_read_b128 v[190:193], v163
	ds_read_b128 v[194:197], v164
	ds_read_b128 v[198:201], v155 offset:32768
	ds_read_b128 v[202:205], v155 offset:34816
	ds_read_b128 v[206:209], v156 offset:32768
	ds_read_b128 v[210:213], v156 offset:34816
	ds_read_b128 v[214:217], v155 offset:36864
	ds_read_b128 v[218:221], v155 offset:38912
	ds_read_b128 v[222:225], v156 offset:36864
	ds_read_b128 v[226:229], v156 offset:38912
	global_load_lds_dwordx4 v[234:235], off
	v_lshl_add_u64 v[234:235], s[34:35], 0, v[130:131]
	s_mov_b32 m0, s40
	s_nop 0
	global_load_lds_dwordx4 v[234:235], off
	s_waitcnt vmcnt(8)
	s_waitcnt lgkmcnt(0)
	s_barrier
	s_setprio 2
	s_waitcnt lgkmcnt(0)
	v_mfma_f32_16x16x32_f16 v[124:127], v[166:169], v[198:201], v[124:127]
	v_mfma_f32_16x16x32_f16 v[124:127], v[170:173], v[206:209], v[124:127]
	v_mfma_f32_16x16x32_f16 v[120:123], v[174:177], v[198:201], v[120:123]
	v_mfma_f32_16x16x32_f16 v[120:123], v[178:181], v[206:209], v[120:123]
	v_mfma_f32_16x16x32_f16 v[116:119], v[166:169], v[202:205], v[116:119]
	v_mfma_f32_16x16x32_f16 v[116:119], v[170:173], v[210:213], v[116:119]
	v_mfma_f32_16x16x32_f16 v[112:115], v[174:177], v[202:205], v[112:115]
	v_mfma_f32_16x16x32_f16 v[112:115], v[178:181], v[210:213], v[112:115]
	v_mfma_f32_16x16x32_f16 v[108:111], v[166:169], v[214:217], v[108:111]
	v_mfma_f32_16x16x32_f16 v[108:111], v[170:173], v[222:225], v[108:111]
	v_mfma_f32_16x16x32_f16 v[100:103], v[174:177], v[214:217], v[100:103]
	v_mfma_f32_16x16x32_f16 v[100:103], v[178:181], v[222:225], v[100:103]
	v_mfma_f32_16x16x32_f16 v[92:95], v[166:169], v[218:221], v[92:95]
	v_mfma_f32_16x16x32_f16 v[92:95], v[170:173], v[226:229], v[92:95]
	v_mfma_f32_16x16x32_f16 v[84:87], v[174:177], v[218:221], v[84:87]
	v_mfma_f32_16x16x32_f16 v[84:87], v[178:181], v[226:229], v[84:87]
	s_setprio 0
	s_setprio 2
	v_mfma_f32_16x16x32_f16 v[104:107], v[182:185], v[198:201], v[104:107]
	v_mfma_f32_16x16x32_f16 v[104:107], v[186:189], v[206:209], v[104:107]
	v_mfma_f32_16x16x32_f16 v[96:99], v[190:193], v[198:201], v[96:99]
	v_mfma_f32_16x16x32_f16 v[96:99], v[194:197], v[206:209], v[96:99]
	v_mfma_f32_16x16x32_f16 v[88:91], v[182:185], v[202:205], v[88:91]
	v_mfma_f32_16x16x32_f16 v[88:91], v[186:189], v[210:213], v[88:91]
	v_mfma_f32_16x16x32_f16 v[80:83], v[190:193], v[202:205], v[80:83]
	v_mfma_f32_16x16x32_f16 v[80:83], v[194:197], v[210:213], v[80:83]
	v_mfma_f32_16x16x32_f16 v[76:79], v[182:185], v[214:217], v[76:79]
	v_mfma_f32_16x16x32_f16 v[76:79], v[186:189], v[222:225], v[76:79]
	v_mfma_f32_16x16x32_f16 v[72:75], v[190:193], v[214:217], v[72:75]
	v_mfma_f32_16x16x32_f16 v[72:75], v[194:197], v[222:225], v[72:75]
	v_mfma_f32_16x16x32_f16 v[68:71], v[182:185], v[218:221], v[68:71]
	v_mfma_f32_16x16x32_f16 v[68:71], v[186:189], v[226:229], v[68:71]
	v_mfma_f32_16x16x32_f16 v[64:67], v[190:193], v[218:221], v[64:67]
	v_mfma_f32_16x16x32_f16 v[64:67], v[194:197], v[226:229], v[64:67]
	s_setprio 0
	s_add_i32 s34, s46, s36
	v_lshl_add_u64 v[138:139], v[138:139], 0, s[14:15]
	s_mov_b32 m0, s34
	ds_read_b128 v[198:201], v155 offset:49152
	ds_read_b128 v[202:205], v155 offset:51200
	ds_read_b128 v[206:209], v156 offset:49152
	ds_read_b128 v[210:213], v156 offset:51200
	ds_read_b128 v[214:217], v155 offset:53248
	ds_read_b128 v[218:221], v155 offset:55296
	ds_read_b128 v[222:225], v156 offset:53248
	ds_read_b128 v[226:229], v156 offset:55296
	global_load_lds_dwordx4 v[138:139], off
	s_add_i32 m0, s34, 0x2000
	s_add_u32 s30, s30, 0x380080
	v_lshl_add_u64 v[138:139], v[144:145], 0, s[14:15]
	s_addc_u32 s31, s31, 0
	s_add_i32 s34, s47, s36
	global_load_lds_dwordx4 v[138:139], off
	v_lshl_add_u64 v[138:139], s[30:31], 0, v[128:129]
	s_mov_b32 m0, s34
	s_nop 0
	global_load_lds_dwordx4 v[138:139], off
	v_lshl_add_u64 v[138:139], s[30:31], 0, v[130:131]
	s_add_i32 m0, s34, 0x2000
	s_nop 0
	global_load_lds_dwordx4 v[138:139], off
	v_lshl_add_u64 v[138:139], v[230:231], 0, s[14:15]
	s_mov_b32 m0, s41
	s_nop 0
	global_load_lds_dwordx4 v[138:139], off
	v_lshl_add_u64 v[138:139], v[232:233], 0, s[14:15]
	s_mov_b32 m0, s42
	s_nop 0
	global_load_lds_dwordx4 v[138:139], off
	s_waitcnt vmcnt(8)
	s_waitcnt lgkmcnt(0)
	s_barrier
	s_setprio 2
	s_waitcnt lgkmcnt(0)
	v_mfma_f32_16x16x32_f16 v[60:63], v[166:169], v[198:201], v[60:63]
	v_mfma_f32_16x16x32_f16 v[60:63], v[170:173], v[206:209], v[60:63]
	v_mfma_f32_16x16x32_f16 v[56:59], v[174:177], v[198:201], v[56:59]
	v_mfma_f32_16x16x32_f16 v[56:59], v[178:181], v[206:209], v[56:59]
	v_mfma_f32_16x16x32_f16 v[52:55], v[166:169], v[202:205], v[52:55]
	v_mfma_f32_16x16x32_f16 v[52:55], v[170:173], v[210:213], v[52:55]
	v_mfma_f32_16x16x32_f16 v[48:51], v[174:177], v[202:205], v[48:51]
	v_mfma_f32_16x16x32_f16 v[48:51], v[178:181], v[210:213], v[48:51]
	v_mfma_f32_16x16x32_f16 v[40:43], v[166:169], v[214:217], v[40:43]
	v_mfma_f32_16x16x32_f16 v[40:43], v[170:173], v[222:225], v[40:43]
	v_mfma_f32_16x16x32_f16 v[32:35], v[174:177], v[214:217], v[32:35]
	v_mfma_f32_16x16x32_f16 v[32:35], v[178:181], v[222:225], v[32:35]
	v_mfma_f32_16x16x32_f16 v[12:15], v[166:169], v[218:221], v[12:15]
	v_mfma_f32_16x16x32_f16 v[12:15], v[170:173], v[226:229], v[12:15]
	v_mfma_f32_16x16x32_f16 v[8:11], v[174:177], v[218:221], v[8:11]
	v_mfma_f32_16x16x32_f16 v[8:11], v[178:181], v[226:229], v[8:11]
	s_setprio 0
	s_setprio 2
	v_mfma_f32_16x16x32_f16 v[44:47], v[182:185], v[198:201], v[44:47]
	v_mfma_f32_16x16x32_f16 v[44:47], v[186:189], v[206:209], v[44:47]
	v_mfma_f32_16x16x32_f16 v[36:39], v[190:193], v[198:201], v[36:39]
	v_mfma_f32_16x16x32_f16 v[36:39], v[194:197], v[206:209], v[36:39]
	v_mfma_f32_16x16x32_f16 v[28:31], v[182:185], v[202:205], v[28:31]
	v_mfma_f32_16x16x32_f16 v[28:31], v[186:189], v[210:213], v[28:31]
	v_mfma_f32_16x16x32_f16 v[24:27], v[190:193], v[202:205], v[24:27]
	v_mfma_f32_16x16x32_f16 v[24:27], v[194:197], v[210:213], v[24:27]
	v_mfma_f32_16x16x32_f16 v[20:23], v[182:185], v[214:217], v[20:23]
	v_mfma_f32_16x16x32_f16 v[20:23], v[186:189], v[222:225], v[20:23]
	v_mfma_f32_16x16x32_f16 v[16:19], v[190:193], v[214:217], v[16:19]
	v_mfma_f32_16x16x32_f16 v[16:19], v[194:197], v[222:225], v[16:19]
	v_mfma_f32_16x16x32_f16 v[4:7], v[182:185], v[218:221], v[4:7]
	v_mfma_f32_16x16x32_f16 v[4:7], v[186:189], v[226:229], v[4:7]
	v_mfma_f32_16x16x32_f16 v[0:3], v[190:193], v[218:221], v[0:3]
	v_mfma_f32_16x16x32_f16 v[0:3], v[194:197], v[226:229], v[0:3]
	s_setprio 0
	s_add_i32 s58, s58, 2
	s_add_u32 s56, s56, 0x100
	s_addc_u32 s57, s57, 0
	s_add_u32 s28, s28, 0x100
	s_addc_u32 s29, s29, 0
	s_cmpk_gt_u32 s58, 0xdd
	s_cbranch_scc0 .Lk2_loopY
